# weight-conversion items: source/destination pointers fetched through the scalar cache (s_load + lgkmcnt) instead of a vector load + vmcnt(0) that also drained the previous item's stores (hook, naw, la
# speedup vs baseline: 1.0153x; 1.0153x over previous
; __device__ __forceinline__ void conv_item8(const float* W, int K, int N, unsigned char* WT, int k0, int n0, int drow0, LAS unsigned* scr, int lane, float sc, bool rperm = false) {
;     const int q = lane >> 4, n4 = lane & 15;
;     f32x4 v[4][4];
; #pragma unroll
;     for (int i = 0; i < 4; ++i)
; #pragma unroll
;         for (int t = 0; t < 4; ++t) v[i][t] = __builtin_nontemporal_load((const f32x4*)(W + (size_t)(k0 + 4 * (4 * i + q) + t) * N + n0 + 4 * n4));
; #pragma unroll
;     for (int i = 0; i < 4; ++i) { const int rp = 4 * i + q; LAS unsigned* sp = scr + (4 * n4) * 17 + rp;
;         sp[0]  = pk4_fp8(v[i][0].x * sc, v[i][1].x * sc, v[i][2].x * sc, v[i][3].x * sc);
;         sp[17] = pk4_fp8(v[i][0].y * sc, v[i][1].y * sc, v[i][2].y * sc, v[i][3].y * sc);
;         sp[34] = pk4_fp8(v[i][0].z * sc, v[i][1].z * sc, v[i][2].z * sc, v[i][3].z * sc);
; __device__ __forceinline__ void conv_dispatch(const Params& p, int it, LAS unsigned* scr, int lane) {
;     using namespace cv;
;     int r = it; const int l = (r >= I_L0) ? 1 : 0; if (l) r -= I_L0;
;     const int i_in = l ? I_IN1 : I_IN0;
;     if (r < i_in) { const int N = l ? ODW : EVW, nb = N / 64;
;         conv_item8(p.in[l ? 16 : 5], D, N, l ? p.wp[IX_WIN1] : p.wp[IX_WIN0], (r / nb) * 64, (r % nb) * 64, (r % nb) * 64, scr, lane, F8_SW, l == 1 && (r % nb) < 64 && ((r % nb) & 1) == 0);
;         return; } r -= i_in;
;     if (r < I_OUT) { if (OUT_F8) conv_item8(p.in[l ? 19 : 8], D, D, l ? p.wp[IX_WOUT1] : p.wp[IX_WOUT0], (r / 32) * 64, (r % 32) * 64, (r % 32) * 64, scr, lane, F8_SWD);
;         else conv_item(p.in[l ? 19 : 8], D, D, (bf16_t*)(l ? p.wp[IX_WOUT1] : p.wp[IX_WOUT0]), (r / 32) * 64, (r % 32) * 64, (r % 32) * 64, scr, lane); return; } r -= I_OUT;
;     if (r < 2 * I_G) { const int up = r >= I_G; if (up) r -= I_G; const int e = r / 512, rr = r % 512, kb = rr / 16, nb = rr % 16, n0 = nb * 64;
;         conv_item8(p.in[(l ? 21 : 10) + up] + (size_t)e * D * DFF, D, DFF, (l ? p.wp[IX_WGU1] : p.wp[IX_WGU0]) + (size_t)e * 2048 * D, kb * 64, n0, (n0 >> 7) * 256 + (n0 & 127) + up * 128, scr, lane, F8_SW);
;         return; } r -= 2 * I_G;
;     { const int e = r / 512, rr = r % 512, kb = rr / 32, nb = rr % 32;
;         conv_item8(p.in[l ? 23 : 12] + (size_t)e * DFF * D, DFF, D, (l ? p.wp[IX_WD1] : p.wp[IX_WD0]) + (size_t)e * D * DFF, kb * 64, nb * 64, nb * 64, scr, lane, F8_SWD); }
.LBB0_157:
	s_movk_i32 s6, 0x4800
	v_cmp_gt_i32_e32 vcc, s6, v67
	s_movk_i32 s6, 0x73ff
	s_nop 0
	v_cndmask_b32_e32 v0, v177, v178, vcc
	v_add_u32_e32 v0, v0, v67
	v_add_u32_e32 v3, 0xffff8c00, v0
	v_cmp_lt_i32_e32 vcc, s6, v0
	s_nop 1
	v_cndmask_b32_e32 v2, v179, v180, vcc
	v_cndmask_b32_e32 v4, v0, v3, vcc
	v_cmp_ge_i32_e64 s[6:7], v4, v2
	s_and_saveexec_b64 s[8:9], s[6:7]
	s_xor_b64 s[8:9], exec, s[8:9]
	s_cbranch_execz .LBB0_167
	v_sub_u32_e32 v5, v4, v2
	s_movk_i32 s6, 0x3ff
	v_cmp_lt_i32_e64 s[6:7], s6, v5
	s_and_saveexec_b64 s[48:49], s[6:7]
	s_xor_b64 s[48:49], exec, s[48:49]
	s_cbranch_execz .LBB0_164
	s_movk_i32 s6, 0x43ff
	v_cmp_lt_u32_e64 s[6:7], s6, v5
	s_and_saveexec_b64 s[50:51], s[6:7]
	s_xor_b64 s[50:51], exec, s[50:51]
	s_cbranch_execz .LBB0_161
	v_cndmask_b32_e32 v162, v181, v182, vcc
	v_lshl_add_u64 v[6:7], s[0:1], 0, v[162:163]
	s_nop 0
	v_readfirstlane_b32 s92, v6
	v_readfirstlane_b32 s93, v7
	s_nop 4
	s_load_dwordx2 s[94:95], s[92:93], 0x0
	v_add_u32_e32 v0, 0xffffbc00, v5
	v_lshrrev_b32_e32 v2, 9, v0
	v_mov_b32_e32 v3, v163
	v_lshlrev_b64 v[8:9], 23, v[2:3]
	v_cndmask_b32_e32 v162, v183, v184, vcc
	v_lshlrev_b32_e32 v0, 1, v4
	v_and_b32_e32 v72, 0x3c0, v0
	v_lshlrev_b32_e32 v0, 6, v4
	v_and_b32_e32 v74, 0x7c0, v0
	v_lshlrev_b64 v[2:3], 21, v[2:3]
	v_mov_b32_e32 v73, v163
	s_waitcnt lgkmcnt(0)
	v_mov_b32_e32 v6, s94
	v_mov_b32_e32 v7, s95
	v_lshl_add_u64 v[6:7], v[6:7], 0, v[8:9]
	v_lshl_add_u64 v[8:9], s[0:1], 0, v[162:163]
	s_nop 0
	v_readfirstlane_b32 s92, v8
	v_readfirstlane_b32 s93, v9
	s_nop 4
	s_load_dwordx2 s[94:95], s[92:93], 0x0
	v_lshlrev_b32_e32 v162, 2, v74
	s_waitcnt lgkmcnt(0)
	v_mov_b32_e32 v8, s94
	v_mov_b32_e32 v9, s95
	v_lshl_add_u64 v[70:71], v[8:9], 0, v[2:3]
	v_lshl_add_u64 v[2:3], v[6:7], 0, v[162:163]
	v_lshlrev_b32_e32 v162, 2, v66
	v_lshl_add_u64 v[2:3], v[2:3], 0, v[162:163]
	v_lshl_or_b32 v162, v72, 13, v86
	v_lshl_add_u64 v[18:19], v[2:3], 0, v[162:163]
	v_add_co_u32_e64 v2, s[6:7], s57, v18
	global_load_dwordx4 v[50:53], v[18:19], off nt
	s_nop 0
	v_addc_co_u32_e64 v3, s[6:7], 0, v19, s[6:7]
	s_movk_i32 s6, 0x4000
	global_load_dwordx4 v[54:57], v[2:3], off nt
	v_add_co_u32_e64 v2, s[6:7], s6, v18
	s_nop 1
	v_addc_co_u32_e64 v3, s[6:7], 0, v19, s[6:7]
	s_movk_i32 s6, 0x6000
	global_load_dwordx4 v[58:61], v[2:3], off nt
	v_add_co_u32_e64 v2, s[6:7], s6, v18
	s_nop 1
	v_addc_co_u32_e64 v3, s[6:7], 0, v19, s[6:7]
	s_mov_b32 s6, 0x20000
	global_load_dwordx4 v[62:65], v[2:3], off nt
	v_add_co_u32_e64 v2, s[6:7], s6, v18
	s_nop 1
	v_addc_co_u32_e64 v3, s[6:7], 0, v19, s[6:7]
	s_mov_b32 s6, 0x22000
	global_load_dwordx4 v[34:37], v[2:3], off nt
	v_add_co_u32_e64 v2, s[6:7], s6, v18
	s_nop 1
	v_addc_co_u32_e64 v3, s[6:7], 0, v19, s[6:7]
	s_mov_b32 s6, 0x24000
	global_load_dwordx4 v[38:41], v[2:3], off nt
	v_add_co_u32_e64 v2, s[6:7], s6, v18
	s_nop 0
	s_nop 0
	v_addc_co_u32_e64 v3, s[6:7], 0, v19, s[6:7]
	s_mov_b32 s6, 0x26000
	global_load_dwordx4 v[42:45], v[2:3], off nt
	v_add_co_u32_e64 v2, s[6:7], s6, v18
	s_nop 0
	s_nop 0
	v_addc_co_u32_e64 v3, s[6:7], 0, v19, s[6:7]
	s_mov_b32 s6, 0x40000
	global_load_dwordx4 v[46:49], v[2:3], off nt
	v_add_co_u32_e64 v2, s[6:7], s6, v18
	s_nop 0
	s_nop 0
	v_addc_co_u32_e64 v3, s[6:7], 0, v19, s[6:7]
	s_mov_b32 s6, 0x42000
	s_nop 0
	v_add_co_u32_e64 v6, s[6:7], s6, v18
	global_load_dwordx4 v[2:5], v[2:3], off nt
	s_nop 0
	v_addc_co_u32_e64 v7, s[6:7], 0, v19, s[6:7]
	global_load_dwordx4 v[22:25], v[6:7], off nt
	v_add_co_u32_e64 v6, s[6:7], s72, v18
	s_nop 0
	s_nop 0
	v_addc_co_u32_e64 v7, s[6:7], 0, v19, s[6:7]
	global_load_dwordx4 v[26:29], v[6:7], off nt
	v_add_co_u32_e64 v6, s[6:7], s73, v18
	s_nop 0
	s_nop 0
	v_addc_co_u32_e64 v7, s[6:7], 0, v19, s[6:7]
	global_load_dwordx4 v[30:33], v[6:7], off nt
	v_add_co_u32_e64 v6, s[6:7], s74, v18
	s_nop 0
	s_nop 0
	v_addc_co_u32_e64 v7, s[6:7], 0, v19, s[6:7]
	v_add_co_u32_e64 v10, s[6:7], s75, v18
	global_load_dwordx4 v[6:9], v[6:7], off nt
	s_nop 0
	v_addc_co_u32_e64 v11, s[6:7], 0, v19, s[6:7]
	global_load_dwordx4 v[10:13], v[10:11], off nt
	v_add_co_u32_e64 v14, s[6:7], s76, v18
	s_nop 0
	s_nop 0
	v_addc_co_u32_e64 v15, s[6:7], 0, v19, s[6:7]
	v_add_co_u32_e64 v18, s[6:7], s77, v18
	global_load_dwordx4 v[14:17], v[14:15], off nt
	s_nop 0
	v_addc_co_u32_e64 v19, s[6:7], 0, v19, s[6:7]
	global_load_dwordx4 v[18:21], v[18:19], off nt
	s_waitcnt vmcnt(15)
	v_mul_f32_e32 v0, 0x43800000, v50
	s_waitcnt vmcnt(14)
	v_mul_f32_e32 v50, 0x43800000, v54
	s_waitcnt vmcnt(13)
	v_mul_f32_e32 v54, 0x43800000, v58
	s_waitcnt vmcnt(12)
	v_mul_f32_e32 v58, 0x43800000, v62
	v_mov_b32_e32 v62, v163
	v_cvt_pk_fp8_f32 v62, v0, v50
	v_mul_f32_e32 v0, 0x43800000, v51
	v_mul_f32_e32 v50, 0x43800000, v55
	v_mov_b32_e32 v55, v163
	v_cvt_pk_fp8_f32 v55, v0, v50
	v_cvt_pk_fp8_f32 v62, v54, v58 op_sel:[0,0,1]
	v_mul_f32_e32 v51, 0x43800000, v59
	v_mul_f32_e32 v54, 0x43800000, v63
	v_cvt_pk_fp8_f32 v55, v51, v54 op_sel:[0,0,1]
	v_mul_f32_e32 v0, 0x43800000, v52
	v_mul_f32_e32 v50, 0x43800000, v56
	v_mov_b32_e32 v54, v163
	v_cvt_pk_fp8_f32 v54, v0, v50
	v_mul_f32_e32 v0, 0x43800000, v53
	v_mul_f32_e32 v50, 0x43800000, v57
	v_mov_b32_e32 v53, v163
	v_cvt_pk_fp8_f32 v53, v0, v50
	v_mul_f32_e32 v51, 0x43800000, v60
	s_waitcnt vmcnt(11)
	v_mul_f32_e32 v0, 0x43800000, v34
	v_mul_f32_e32 v52, 0x43800000, v64
	v_cvt_pk_fp8_f32 v54, v51, v52 op_sel:[0,0,1]
	v_mul_f32_e32 v51, 0x43800000, v61
	v_mul_f32_e32 v52, 0x43800000, v65
	v_cvt_pk_fp8_f32 v53, v51, v52 op_sel:[0,0,1]
	s_waitcnt vmcnt(10)
	v_mul_f32_e32 v34, 0x43800000, v38
	s_waitcnt vmcnt(9)
	v_mul_f32_e32 v38, 0x43800000, v42
	s_waitcnt vmcnt(8)
; #define LAS __attribute__((address_space(3)))
; __device__ __forceinline__ unsigned pk4_fp8(float a, float b, float c, float d) { unsigned w = 0u; w = __builtin_amdgcn_cvt_pk_fp8_f32(a, b, w, false); w = __builtin_amdgcn_cvt_pk_fp8_f32(c, d, w, true); return w; }
; __device__ __forceinline__ void conv_item8(const float* W, int K, int N, unsigned char* WT, int k0, int n0, int drow0, LAS unsigned* scr, int lane, float sc, bool rperm = false) {
;     ...
; #pragma unroll
;     for (int i = 0; i < 4; ++i) { const int rp = 4 * i + q; LAS unsigned* sp = scr + (4 * n4) * 17 + rp;
;         sp[0]  = pk4_fp8(v[i][0].x * sc, v[i][1].x * sc, v[i][2].x * sc, v[i][3].x * sc);
;         sp[17] = pk4_fp8(v[i][0].y * sc, v[i][1].y * sc, v[i][2].y * sc, v[i][3].y * sc);
;         sp[34] = pk4_fp8(v[i][0].z * sc, v[i][1].z * sc, v[i][2].z * sc, v[i][3].z * sc);
;         sp[51] = pk4_fp8(v[i][0].w * sc, v[i][1].w * sc, v[i][2].w * sc, v[i][3].w * sc); }
;     asm volatile("s_waitcnt lgkmcnt(0)" ::: "memory");
;     const int c = lane & 3;
; #pragma unroll
;     for (int j = 0; j < 4; ++j) {
;         const int n = (lane >> 2) + 16 * j; const LAS unsigned* sp = scr + n * 17 + 4 * c;
;         u32x4 o; o.x = sp[0]; o.y = sp[1]; o.z = sp[2]; o.w = sp[3];
;         const int nr = (rperm && n < 32) ? ((n < 16) ? 2 * n : 2 * (n - 16) + 1) : n;
;         *(u32x4*)(WT + (size_t)(drow0 + nr) * K + k0 + 16 * c) = o;
;     }
;     asm volatile("s_waitcnt lgkmcnt(0)" ::: "memory");
	v_mul_f32_e32 v42, 0x43800000, v46
	v_mov_b32_e32 v46, v163
	v_cvt_pk_fp8_f32 v46, v0, v34
	v_mul_f32_e32 v0, 0x43800000, v35
	v_mul_f32_e32 v34, 0x43800000, v39
	v_mov_b32_e32 v39, v163
	v_cvt_pk_fp8_f32 v39, v0, v34
	v_cvt_pk_fp8_f32 v46, v38, v42 op_sel:[0,0,1]
	v_mul_f32_e32 v35, 0x43800000, v43
	v_mul_f32_e32 v38, 0x43800000, v47
	v_cvt_pk_fp8_f32 v39, v35, v38 op_sel:[0,0,1]
	v_mul_f32_e32 v0, 0x43800000, v36
	v_mul_f32_e32 v34, 0x43800000, v40
	v_mov_b32_e32 v38, v163
	v_cvt_pk_fp8_f32 v38, v0, v34
	v_mul_f32_e32 v0, 0x43800000, v37
	v_mul_f32_e32 v34, 0x43800000, v41
	v_mov_b32_e32 v37, v163
	v_cvt_pk_fp8_f32 v37, v0, v34
	s_waitcnt vmcnt(7)
	v_mul_f32_e32 v0, 0x43800000, v2
	s_waitcnt vmcnt(6)
	v_mul_f32_e32 v2, 0x43800000, v22
	s_waitcnt vmcnt(5)
	v_mul_f32_e32 v22, 0x43800000, v26
	v_mul_f32_e32 v35, 0x43800000, v44
	v_mul_f32_e32 v36, 0x43800000, v48
	s_waitcnt vmcnt(4)
	v_mul_f32_e32 v26, 0x43800000, v30
	v_mov_b32_e32 v30, v163
	v_cvt_pk_fp8_f32 v30, v0, v2
	v_mul_f32_e32 v0, 0x43800000, v3
	v_mul_f32_e32 v2, 0x43800000, v23
	v_mov_b32_e32 v23, v163
	v_cvt_pk_fp8_f32 v23, v0, v2
	v_cvt_pk_fp8_f32 v30, v22, v26 op_sel:[0,0,1]
	v_mul_f32_e32 v3, 0x43800000, v27
	v_mul_f32_e32 v22, 0x43800000, v31
	v_cvt_pk_fp8_f32 v23, v3, v22 op_sel:[0,0,1]
	v_mul_f32_e32 v0, 0x43800000, v4
	v_mul_f32_e32 v2, 0x43800000, v24
	v_mov_b32_e32 v22, v163
	v_cvt_pk_fp8_f32 v22, v0, v2
	v_mul_f32_e32 v0, 0x43800000, v5
	v_mul_f32_e32 v2, 0x43800000, v25
	v_mov_b32_e32 v5, v163
	v_cvt_pk_fp8_f32 v5, v0, v2
	s_waitcnt vmcnt(3)
	v_mul_f32_e32 v0, 0x43800000, v6
	s_waitcnt vmcnt(2)
	v_mul_f32_e32 v2, 0x43800000, v10
	v_mov_b32_e32 v6, v163
	v_cvt_pk_fp8_f32 v6, v0, v2
	v_mul_f32_e32 v3, 0x43800000, v28
	v_mul_f32_e32 v4, 0x43800000, v32
	v_cvt_pk_fp8_f32 v22, v3, v4 op_sel:[0,0,1]
	v_mul_f32_e32 v3, 0x43800000, v29
	v_mul_f32_e32 v4, 0x43800000, v33
	v_cvt_pk_fp8_f32 v5, v3, v4 op_sel:[0,0,1]
	s_waitcnt vmcnt(1)
	v_mul_f32_e32 v3, 0x43800000, v14
	s_waitcnt vmcnt(0)
	v_mul_f32_e32 v4, 0x43800000, v18
	v_cvt_pk_fp8_f32 v6, v3, v4 op_sel:[0,0,1]
	v_mul_f32_e32 v0, 0x43800000, v7
	v_mul_f32_e32 v2, 0x43800000, v11
	v_mul_f32_e32 v3, 0x43800000, v15
	ds_write2_b32 v78, v30, v6 offset0:8 offset1:12
	v_mov_b32_e32 v6, v163
	v_cvt_pk_fp8_f32 v6, v0, v2
	v_mul_f32_e32 v4, 0x43800000, v19
	v_mul_f32_e32 v0, 0x43800000, v8
	v_mul_f32_e32 v2, 0x43800000, v12
	v_cvt_pk_fp8_f32 v6, v3, v4 op_sel:[0,0,1]
	v_mul_f32_e32 v3, 0x43800000, v16
	v_mul_f32_e32 v4, 0x43800000, v20
	v_cvt_pk_fp8_f32 v38, v35, v36 op_sel:[0,0,1]
	ds_write2_b32 v78, v23, v6 offset0:25 offset1:29
	v_mov_b32_e32 v6, v163
	v_cvt_pk_fp8_f32 v6, v0, v2
	v_mul_f32_e32 v0, 0x43800000, v9
	v_mul_f32_e32 v2, 0x43800000, v13
	v_mul_f32_e32 v35, 0x43800000, v45
	v_cvt_pk_fp8_f32 v6, v3, v4 op_sel:[0,0,1]
	v_mul_f32_e32 v36, 0x43800000, v49
	v_mul_f32_e32 v3, 0x43800000, v17
	v_mul_f32_e32 v4, 0x43800000, v21
	ds_write2_b32 v78, v22, v6 offset0:42 offset1:46
	v_mov_b32_e32 v6, v163
	v_cvt_pk_fp8_f32 v6, v0, v2
	v_cvt_pk_fp8_f32 v37, v35, v36 op_sel:[0,0,1]
	ds_write2_b32 v78, v62, v46 offset1:4
	ds_write2_b32 v78, v55, v39 offset0:17 offset1:21
	v_cvt_pk_fp8_f32 v6, v3, v4 op_sel:[0,0,1]
	ds_write2_b32 v78, v54, v38 offset0:34 offset1:38
	ds_write2_b32 v78, v53, v37 offset0:51 offset1:55
	v_lshl_add_u64 v[2:3], v[70:71], 0, v[72:73]
	ds_write2_b32 v78, v5, v6 offset0:59 offset1:63
	s_waitcnt lgkmcnt(0)
	v_add_u32_e32 v0, v80, v81
	v_lshl_add_u64 v[6:7], v[2:3], 0, v[68:69]
	ds_read2_b32 v[2:3], v0 offset1:1
	ds_read2_b32 v[4:5], v0 offset0:2 offset1:3
	v_or_b32_e32 v8, v74, v79
	v_lshlrev_b32_e32 v162, 10, v8
	v_lshl_add_u64 v[8:9], v[6:7], 0, v[162:163]
	s_waitcnt lgkmcnt(0)
	global_store_dwordx4 v[8:9], v[2:5], off
	v_or_b32_e32 v8, v74, v82
	s_nop 0
	v_add_u32_e32 v2, 0x440, v0
	v_add_u32_e32 v4, 0x448, v0
	ds_read2_b32 v[2:3], v2 offset1:1
	ds_read2_b32 v[4:5], v4 offset1:1
	v_lshlrev_b32_e32 v162, 10, v8
	v_lshl_add_u64 v[8:9], v[6:7], 0, v[162:163]
	s_waitcnt lgkmcnt(0)
	global_store_dwordx4 v[8:9], v[2:5], off
	s_nop 1
	v_add_u32_e32 v2, 0x880, v0
	v_add_u32_e32 v4, 0x888, v0
	ds_read2_b32 v[2:3], v2 offset1:1
	ds_read2_b32 v[4:5], v4 offset1:1
	v_or_b32_e32 v8, v74, v83
	v_lshlrev_b32_e32 v162, 10, v8
	v_lshl_add_u64 v[8:9], v[6:7], 0, v[162:163]
	s_waitcnt lgkmcnt(0)
	global_store_dwordx4 v[8:9], v[2:5], off
	s_nop 1
	v_add_u32_e32 v2, 0xcc0, v0
	v_add_u32_e32 v0, 0xcc8, v0
	ds_read2_b32 v[2:3], v2 offset1:1
	ds_read2_b32 v[4:5], v0 offset1:1
	v_or_b32_e32 v0, v74, v84
	v_lshlrev_b32_e32 v162, 10, v0
	v_lshl_add_u64 v[6:7], v[6:7], 0, v[162:163]
	s_waitcnt lgkmcnt(0)
	global_store_dwordx4 v[6:7], v[2:5], off
	s_waitcnt lgkmcnt(0)
; #define LAS __attribute__((address_space(3)))
; __device__ __forceinline__ unsigned pk4_fp8(float a, float b, float c, float d) { unsigned w = 0u; w = __builtin_amdgcn_cvt_pk_fp8_f32(a, b, w, false); w = __builtin_amdgcn_cvt_pk_fp8_f32(c, d, w, true); return w; }
; __device__ __forceinline__ void conv_item8(const float* W, int K, int N, unsigned char* WT, int k0, int n0, int drow0, LAS unsigned* scr, int lane, float sc, bool rperm = false) {
;     const int q = lane >> 4, n4 = lane & 15;
;     f32x4 v[4][4];
; #pragma unroll
;     for (int i = 0; i < 4; ++i)
; #pragma unroll
;         for (int t = 0; t < 4; ++t) v[i][t] = __builtin_nontemporal_load((const f32x4*)(W + (size_t)(k0 + 4 * (4 * i + q) + t) * N + n0 + 4 * n4));
; #pragma unroll
;     for (int i = 0; i < 4; ++i) { const int rp = 4 * i + q; LAS unsigned* sp = scr + (4 * n4) * 17 + rp;
;         sp[0]  = pk4_fp8(v[i][0].x * sc, v[i][1].x * sc, v[i][2].x * sc, v[i][3].x * sc);
;         sp[17] = pk4_fp8(v[i][0].y * sc, v[i][1].y * sc, v[i][2].y * sc, v[i][3].y * sc);
;         sp[34] = pk4_fp8(v[i][0].z * sc, v[i][1].z * sc, v[i][2].z * sc, v[i][3].z * sc);
;         sp[51] = pk4_fp8(v[i][0].w * sc, v[i][1].w * sc, v[i][2].w * sc, v[i][3].w * sc); }
; __device__ __forceinline__ void conv_dispatch(const Params& p, int it, LAS unsigned* scr, int lane) {
;     ...
;     if (r < 2 * I_G) { const int up = r >= I_G; if (up) r -= I_G; const int e = r / 512, rr = r % 512, kb = rr / 16, nb = rr % 16, n0 = nb * 64;
;         conv_item8(p.in[(l ? 21 : 10) + up] + (size_t)e * D * DFF, D, DFF, (l ? p.wp[IX_WGU1] : p.wp[IX_WGU0]) + (size_t)e * 2048 * D, kb * 64, n0, (n0 >> 7) * 256 + (n0 & 127) + up * 128, scr, lane, F8_SW);
.LBB0_161:
	s_andn2_saveexec_b64 s[50:51], s[50:51]
	s_cbranch_execz .LBB0_163
	v_cmp_lt_u32_e64 s[6:7], s78, v5
	v_cndmask_b32_e32 v162, v187, v188, vcc
	v_lshl_add_u64 v[6:7], s[0:1], 0, v[162:163]
	v_cndmask_b32_e64 v3, 0, 1, s[6:7]
	v_lshlrev_b32_e32 v162, 3, v3
	v_lshl_add_u64 v[6:7], v[6:7], 0, v[162:163]
	s_nop 0
	v_readfirstlane_b32 s92, v6
	v_readfirstlane_b32 s93, v7
	s_nop 4
	s_load_dwordx2 s[94:95], s[92:93], 0x0
	v_cndmask_b32_e64 v0, v185, v186, s[6:7]
	v_add_u32_e32 v0, v0, v5
	v_lshrrev_b32_e32 v2, 9, v0
	v_mov_b32_e32 v3, v163
	v_lshlrev_b64 v[8:9], 23, v[2:3]
	v_cndmask_b32_e32 v162, v189, v190, vcc
	v_lshlrev_b64 v[2:3], 22, v[2:3]
	v_lshlrev_b32_e32 v5, 6, v0
	v_and_or_b32 v4, v4, s79, v76
	v_mov_b32_e32 v65, v163
	s_waitcnt lgkmcnt(0)
	v_mov_b32_e32 v6, s94
	v_mov_b32_e32 v7, s95
	v_lshl_add_u64 v[6:7], v[6:7], 0, v[8:9]
	v_lshl_add_u64 v[8:9], s[0:1], 0, v[162:163]
	s_nop 0
	v_readfirstlane_b32 s92, v8
	v_readfirstlane_b32 s93, v9
	s_nop 4
	s_load_dwordx2 s[94:95], s[92:93], 0x0
	s_waitcnt lgkmcnt(0)
	v_mov_b32_e32 v8, s94
	v_mov_b32_e32 v9, s95
	v_lshl_add_u64 v[62:63], v[8:9], 0, v[2:3]
	v_lshlrev_b32_e32 v2, 2, v0
	v_and_b32_e32 v64, 0x7c0, v2
	v_lshlrev_b32_e32 v2, 7, v0
	v_lshlrev_b32_e32 v0, 8, v0
	v_and_b32_e32 v2, 0x700, v2
	v_and_b32_e32 v3, 64, v5
	v_cndmask_b32_e64 v5, 0, v191, s[6:7]
	v_and_b32_e32 v162, 0xf00, v0
	v_or3_b32 v70, v3, v5, v2
	v_lshl_add_u64 v[2:3], v[6:7], 0, v[162:163]
	v_lshlrev_b32_e32 v162, 2, v66
	v_lshl_add_u64 v[2:3], v[2:3], 0, v[162:163]
	v_lshlrev_b32_e32 v162, 14, v4
	v_lshl_add_u64 v[10:11], v[2:3], 0, v[162:163]
	v_add_co_u32_e64 v2, s[6:7], s57, v10
	global_load_dwordx4 v[50:53], v[10:11], off nt
	s_nop 0
	v_addc_co_u32_e64 v3, s[6:7], 0, v11, s[6:7]
	global_load_dwordx4 v[54:57], v[2:3], off offset:-4096 nt
	global_load_dwordx4 v[58:61], v[2:3], off nt
	s_movk_i32 s6, 0x3000
	v_add_co_u32_e64 v2, s[6:7], s6, v10
	s_nop 1
	v_addc_co_u32_e64 v3, s[6:7], 0, v11, s[6:7]
	global_load_dwordx4 v[72:75], v[2:3], off nt
	v_add_co_u32_e64 v2, s[6:7], s80, v10
	s_nop 1
	v_addc_co_u32_e64 v3, s[6:7], 0, v11, s[6:7]
	global_load_dwordx4 v[34:37], v[2:3], off offset:-4096 nt
	global_load_dwordx4 v[38:41], v[2:3], off nt
	v_add_co_u32_e64 v2, s[6:7], s81, v10
	s_nop 0
	s_nop 0
	v_addc_co_u32_e64 v3, s[6:7], 0, v11, s[6:7]
	global_load_dwordx4 v[42:45], v[2:3], off offset:-4096 nt
	global_load_dwordx4 v[46:49], v[2:3], off nt
	v_add_co_u32_e64 v2, s[6:7], s82, v10
	s_nop 0
	s_nop 0
	v_addc_co_u32_e64 v3, s[6:7], 0, v11, s[6:7]
	global_load_dwordx4 v[18:21], v[2:3], off offset:-4096 nt
	global_load_dwordx4 v[22:25], v[2:3], off nt
	v_add_co_u32_e64 v2, s[6:7], s83, v10
	s_nop 0
	s_nop 0
	v_addc_co_u32_e64 v3, s[6:7], 0, v11, s[6:7]
	global_load_dwordx4 v[26:29], v[2:3], off offset:-4096 nt
	global_load_dwordx4 v[30:33], v[2:3], off nt
	v_add_co_u32_e64 v6, s[6:7], s84, v10
	s_nop 0
	s_nop 0
	v_addc_co_u32_e64 v7, s[6:7], 0, v11, s[6:7]
	v_add_co_u32_e64 v14, s[6:7], s85, v10
	global_load_dwordx4 v[2:5], v[6:7], off offset:-4096 nt
	s_nop 0
	global_load_dwordx4 v[6:9], v[6:7], off nt
	v_addc_co_u32_e64 v15, s[6:7], 0, v11, s[6:7]
	global_load_dwordx4 v[10:13], v[14:15], off offset:-4096 nt
	s_nop 0
	global_load_dwordx4 v[14:17], v[14:15], off nt
	s_waitcnt vmcnt(15)
	v_mul_f32_e32 v0, 0x43800000, v50
	s_waitcnt vmcnt(14)
	v_mul_f32_e32 v50, 0x43800000, v54
	v_cvt_pk_fp8_f32 v65, v0, v50
	v_mul_f32_e32 v0, 0x43800000, v51
	v_mul_f32_e32 v50, 0x43800000, v55
	v_mov_b32_e32 v55, v163
	v_cvt_pk_fp8_f32 v55, v0, v50
	s_waitcnt vmcnt(13)
	v_mul_f32_e32 v54, 0x43800000, v58
	v_mul_f32_e32 v51, 0x43800000, v59
	v_mul_f32_e32 v0, 0x43800000, v52
	v_mul_f32_e32 v50, 0x43800000, v56
	s_waitcnt vmcnt(12)
	v_mul_f32_e32 v58, 0x43800000, v72
	v_cvt_pk_fp8_f32 v65, v54, v58 op_sel:[0,0,1]
	v_mul_f32_e32 v54, 0x43800000, v73
	v_cvt_pk_fp8_f32 v55, v51, v54 op_sel:[0,0,1]
	v_mov_b32_e32 v54, v163
	v_cvt_pk_fp8_f32 v54, v0, v50
	v_mul_f32_e32 v0, 0x43800000, v53
	v_mul_f32_e32 v50, 0x43800000, v57
	v_mov_b32_e32 v53, v163
	v_cvt_pk_fp8_f32 v53, v0, v50
	s_waitcnt vmcnt(11)
	v_mul_f32_e32 v0, 0x43800000, v34
	s_waitcnt vmcnt(10)
	v_mul_f32_e32 v34, 0x43800000, v38
	s_waitcnt vmcnt(9)
	v_mul_f32_e32 v38, 0x43800000, v42
	s_waitcnt vmcnt(8)
	v_mul_f32_e32 v42, 0x43800000, v46
	v_mov_b32_e32 v46, v163
	v_cvt_pk_fp8_f32 v46, v0, v34
	v_mul_f32_e32 v0, 0x43800000, v35
	v_mul_f32_e32 v34, 0x43800000, v39
	v_mov_b32_e32 v39, v163
	v_cvt_pk_fp8_f32 v39, v0, v34
	v_cvt_pk_fp8_f32 v46, v38, v42 op_sel:[0,0,1]
	v_mul_f32_e32 v35, 0x43800000, v43
	v_mul_f32_e32 v38, 0x43800000, v47
	v_cvt_pk_fp8_f32 v39, v35, v38 op_sel:[0,0,1]
	v_mul_f32_e32 v0, 0x43800000, v36
	v_mul_f32_e32 v34, 0x43800000, v40
	v_mov_b32_e32 v38, v163
	v_cvt_pk_fp8_f32 v38, v0, v34
	v_mul_f32_e32 v0, 0x43800000, v37
	v_mul_f32_e32 v34, 0x43800000, v41
	v_mov_b32_e32 v37, v163
	v_cvt_pk_fp8_f32 v37, v0, v34
	s_waitcnt vmcnt(7)
; #define LAS __attribute__((address_space(3)))
; __device__ __forceinline__ unsigned pk4_fp8(float a, float b, float c, float d) { unsigned w = 0u; w = __builtin_amdgcn_cvt_pk_fp8_f32(a, b, w, false); w = __builtin_amdgcn_cvt_pk_fp8_f32(c, d, w, true); return w; }
; __device__ __forceinline__ void conv_item8(const float* W, int K, int N, unsigned char* WT, int k0, int n0, int drow0, LAS unsigned* scr, int lane, float sc, bool rperm = false) {
;     ...
; #pragma unroll
;     for (int i = 0; i < 4; ++i) { const int rp = 4 * i + q; LAS unsigned* sp = scr + (4 * n4) * 17 + rp;
;         sp[0]  = pk4_fp8(v[i][0].x * sc, v[i][1].x * sc, v[i][2].x * sc, v[i][3].x * sc);
;         sp[17] = pk4_fp8(v[i][0].y * sc, v[i][1].y * sc, v[i][2].y * sc, v[i][3].y * sc);
;         sp[34] = pk4_fp8(v[i][0].z * sc, v[i][1].z * sc, v[i][2].z * sc, v[i][3].z * sc);
;         sp[51] = pk4_fp8(v[i][0].w * sc, v[i][1].w * sc, v[i][2].w * sc, v[i][3].w * sc); }
;     asm volatile("s_waitcnt lgkmcnt(0)" ::: "memory");
;     const int c = lane & 3;
; #pragma unroll
;     for (int j = 0; j < 4; ++j) {
;         const int n = (lane >> 2) + 16 * j; const LAS unsigned* sp = scr + n * 17 + 4 * c;
;         u32x4 o; o.x = sp[0]; o.y = sp[1]; o.z = sp[2]; o.w = sp[3];
;         const int nr = (rperm && n < 32) ? ((n < 16) ? 2 * n : 2 * (n - 16) + 1) : n;
;         *(u32x4*)(WT + (size_t)(drow0 + nr) * K + k0 + 16 * c) = o;
;     }
;     asm volatile("s_waitcnt lgkmcnt(0)" ::: "memory");
	v_mul_f32_e32 v0, 0x43800000, v18
	s_waitcnt vmcnt(6)
	v_mul_f32_e32 v18, 0x43800000, v22
	s_waitcnt vmcnt(5)
	v_mul_f32_e32 v22, 0x43800000, v26
	s_waitcnt vmcnt(4)
	v_mul_f32_e32 v26, 0x43800000, v30
	v_mov_b32_e32 v30, v163
	v_cvt_pk_fp8_f32 v30, v0, v18
	v_mul_f32_e32 v0, 0x43800000, v19
	v_mul_f32_e32 v19, 0x43800000, v23
	v_mov_b32_e32 v18, v163
	v_cvt_pk_fp8_f32 v18, v0, v19
	v_cvt_pk_fp8_f32 v30, v22, v26 op_sel:[0,0,1]
	v_mul_f32_e32 v22, 0x43800000, v27
	v_mul_f32_e32 v23, 0x43800000, v31
	v_cvt_pk_fp8_f32 v18, v22, v23 op_sel:[0,0,1]
	v_mul_f32_e32 v0, 0x43800000, v20
	v_mul_f32_e32 v19, 0x43800000, v24
	v_mov_b32_e32 v23, v163
	v_cvt_pk_fp8_f32 v23, v0, v19
	v_mul_f32_e32 v20, 0x43800000, v28
	v_mul_f32_e32 v22, 0x43800000, v32
	v_mul_f32_e32 v0, 0x43800000, v21
	v_cvt_pk_fp8_f32 v23, v20, v22 op_sel:[0,0,1]
	v_mul_f32_e32 v20, 0x43800000, v25
	v_mov_b32_e32 v19, v163
	v_cvt_pk_fp8_f32 v19, v0, v20
	s_waitcnt vmcnt(3)
	v_mul_f32_e32 v0, 0x43800000, v2
	s_waitcnt vmcnt(2)
	v_mul_f32_e32 v2, 0x43800000, v6
	s_waitcnt vmcnt(1)
	v_mul_f32_e32 v6, 0x43800000, v10
	s_waitcnt vmcnt(0)
	v_mul_f32_e32 v10, 0x43800000, v14
	v_mov_b32_e32 v14, v163
	v_cvt_pk_fp8_f32 v14, v0, v2
	v_mul_f32_e32 v0, 0x43800000, v3
	v_mul_f32_e32 v2, 0x43800000, v7
	v_mov_b32_e32 v7, v163
	v_cvt_pk_fp8_f32 v7, v0, v2
	v_cvt_pk_fp8_f32 v14, v6, v10 op_sel:[0,0,1]
	v_mul_f32_e32 v3, 0x43800000, v11
	v_mul_f32_e32 v6, 0x43800000, v15
	v_cvt_pk_fp8_f32 v7, v3, v6 op_sel:[0,0,1]
	v_mul_f32_e32 v0, 0x43800000, v4
	v_mul_f32_e32 v2, 0x43800000, v8
	v_mov_b32_e32 v6, v163
	v_cvt_pk_fp8_f32 v6, v0, v2
	v_mul_f32_e32 v0, 0x43800000, v5
	v_mul_f32_e32 v2, 0x43800000, v9
	v_mov_b32_e32 v5, v163
	v_cvt_pk_fp8_f32 v5, v0, v2
	v_mul_f32_e32 v51, 0x43800000, v60
	v_mul_f32_e32 v52, 0x43800000, v74
	v_mul_f32_e32 v35, 0x43800000, v44
	v_mul_f32_e32 v36, 0x43800000, v48
	v_mul_f32_e32 v3, 0x43800000, v12
	v_mul_f32_e32 v4, 0x43800000, v16
	v_cvt_pk_fp8_f32 v54, v51, v52 op_sel:[0,0,1]
	v_mul_f32_e32 v51, 0x43800000, v61
	v_mul_f32_e32 v52, 0x43800000, v75
	v_cvt_pk_fp8_f32 v38, v35, v36 op_sel:[0,0,1]
	v_mul_f32_e32 v35, 0x43800000, v45
	v_mul_f32_e32 v36, 0x43800000, v49
	v_mul_f32_e32 v21, 0x43800000, v29
	v_mul_f32_e32 v22, 0x43800000, v33
	v_cvt_pk_fp8_f32 v6, v3, v4 op_sel:[0,0,1]
	v_mul_f32_e32 v3, 0x43800000, v13
	v_mul_f32_e32 v4, 0x43800000, v17
	v_cvt_pk_fp8_f32 v53, v51, v52 op_sel:[0,0,1]
	v_cvt_pk_fp8_f32 v37, v35, v36 op_sel:[0,0,1]
	v_cvt_pk_fp8_f32 v19, v21, v22 op_sel:[0,0,1]
	v_cvt_pk_fp8_f32 v5, v3, v4 op_sel:[0,0,1]
	ds_write2_b32 v78, v65, v46 offset1:4
	ds_write2_b32 v78, v55, v39 offset0:17 offset1:21
	ds_write2_b32 v78, v54, v38 offset0:34 offset1:38
	ds_write2_b32 v78, v53, v37 offset0:51 offset1:55
	ds_write2_b32 v78, v30, v14 offset0:8 offset1:12
	ds_write2_b32 v78, v18, v7 offset0:25 offset1:29
	ds_write2_b32 v78, v23, v6 offset0:42 offset1:46
	ds_write2_b32 v78, v19, v5 offset0:59 offset1:63
	v_mov_b32_e32 v65, v163
	s_waitcnt lgkmcnt(0)
	v_lshl_add_u64 v[2:3], v[62:63], 0, v[64:65]
	v_add_u32_e32 v0, v80, v81
	v_lshl_add_u64 v[6:7], v[2:3], 0, v[68:69]
	ds_read2_b32 v[2:3], v0 offset1:1
	ds_read2_b32 v[4:5], v0 offset0:2 offset1:3
	v_or_b32_e32 v8, v70, v79
	v_lshlrev_b32_e32 v162, 11, v8
	v_lshl_add_u64 v[8:9], v[6:7], 0, v[162:163]
	s_waitcnt lgkmcnt(0)
	global_store_dwordx4 v[8:9], v[2:5], off
	v_or_b32_e32 v8, v70, v82
	s_nop 0
	v_add_u32_e32 v2, 0x440, v0
	v_add_u32_e32 v4, 0x448, v0
	ds_read2_b32 v[2:3], v2 offset1:1
	ds_read2_b32 v[4:5], v4 offset1:1
	v_lshlrev_b32_e32 v162, 11, v8
	v_lshl_add_u64 v[8:9], v[6:7], 0, v[162:163]
	s_waitcnt lgkmcnt(0)
	global_store_dwordx4 v[8:9], v[2:5], off
	s_nop 1
	v_add_u32_e32 v2, 0x880, v0
	v_add_u32_e32 v4, 0x888, v0
	ds_read2_b32 v[2:3], v2 offset1:1
	ds_read2_b32 v[4:5], v4 offset1:1
	v_or_b32_e32 v8, v70, v83
	v_lshlrev_b32_e32 v162, 11, v8
	v_lshl_add_u64 v[8:9], v[6:7], 0, v[162:163]
	s_waitcnt lgkmcnt(0)
	global_store_dwordx4 v[8:9], v[2:5], off
	s_nop 1
	v_add_u32_e32 v2, 0xcc0, v0
	v_add_u32_e32 v0, 0xcc8, v0
	ds_read2_b32 v[2:3], v2 offset1:1
	ds_read2_b32 v[4:5], v0 offset1:1
	v_or_b32_e32 v0, v70, v84
	v_lshlrev_b32_e32 v162, 11, v0
	v_lshl_add_u64 v[6:7], v[6:7], 0, v[162:163]
	s_waitcnt lgkmcnt(0)
	global_store_dwordx4 v[6:7], v[2:5], off
	s_waitcnt lgkmcnt(0)

; #define LAS __attribute__((address_space(3)))
; __device__ __forceinline__ unsigned pk4_fp8(float a, float b, float c, float d) { unsigned w = 0u; w = __builtin_amdgcn_cvt_pk_fp8_f32(a, b, w, false); w = __builtin_amdgcn_cvt_pk_fp8_f32(c, d, w, true); return w; }
; __device__ __forceinline__ void conv_item8(const float* W, int K, int N, unsigned char* WT, int k0, int n0, int drow0, LAS unsigned* scr, int lane, float sc, bool rperm = false) {
;     const int q = lane >> 4, n4 = lane & 15;
;     f32x4 v[4][4];
; #pragma unroll
;     for (int i = 0; i < 4; ++i)
; #pragma unroll
;         for (int t = 0; t < 4; ++t) v[i][t] = __builtin_nontemporal_load((const f32x4*)(W + (size_t)(k0 + 4 * (4 * i + q) + t) * N + n0 + 4 * n4));
; #pragma unroll
;     for (int i = 0; i < 4; ++i) { const int rp = 4 * i + q; LAS unsigned* sp = scr + (4 * n4) * 17 + rp;
;         sp[0]  = pk4_fp8(v[i][0].x * sc, v[i][1].x * sc, v[i][2].x * sc, v[i][3].x * sc);
;         sp[17] = pk4_fp8(v[i][0].y * sc, v[i][1].y * sc, v[i][2].y * sc, v[i][3].y * sc);
;         sp[34] = pk4_fp8(v[i][0].z * sc, v[i][1].z * sc, v[i][2].z * sc, v[i][3].z * sc);
;         sp[51] = pk4_fp8(v[i][0].w * sc, v[i][1].w * sc, v[i][2].w * sc, v[i][3].w * sc); }
; __device__ __forceinline__ void conv_dispatch(const Params& p, int it, LAS unsigned* scr, int lane) {
;     ...
;     if (r < 2 * I_G) { const int up = r >= I_G; if (up) r -= I_G; const int e = r / 512, rr = r % 512, kb = rr / 16, nb = rr % 16, n0 = nb * 64;
;         conv_item8(p.in[(l ? 21 : 10) + up] + (size_t)e * D * DFF, D, DFF, (l ? p.wp[IX_WGU1] : p.wp[IX_WGU0]) + (size_t)e * 2048 * D, kb * 64, n0, (n0 >> 7) * 256 + (n0 & 127) + up * 128, scr, lane, F8_SW);
.LBB0_317:
	s_andn2_saveexec_b64 s[36:37], s[4:5]
	s_cbranch_execz .LBB0_319
	v_cmp_lt_u32_e32 vcc, s59, v2
	v_mov_b32_e32 v103, v3
	v_and_or_b32 v42, v1, s61, v20
	v_cndmask_b32_e32 v2, v39, v40, vcc
	v_lshl_add_u64 v[16:17], s[0:1], 0, v[2:3]
	s_nop 0
	v_readfirstlane_b32 s76, v16
	v_readfirstlane_b32 s77, v17
	s_nop 4
	s_load_dwordx2 s[78:79], s[76:77], 0x0
	v_cndmask_b32_e32 v0, v37, v38, vcc
	v_add3_u32 v0, v0, v1, s42
	v_lshrrev_b32_e32 v102, 9, v0
	v_lshlrev_b32_e32 v2, 8, v0
	v_lshlrev_b64 v[18:19], 23, v[102:103]
	v_and_b32_e32 v2, 0xf00, v2
	v_mov_b32_e32 v15, v3
	v_mov_b32_e32 v107, v3
	v_mov_b32_e32 v108, v3
	v_mov_b32_e32 v105, v3
	v_mov_b32_e32 v109, v3
	v_mov_b32_e32 v106, v3
	v_mov_b32_e32 v110, v3
	v_mov_b32_e32 v111, v3
	v_mov_b32_e32 v115, v3
	v_mov_b32_e32 v112, v3
	v_mov_b32_e32 v116, v3
	v_mov_b32_e32 v113, v3
	v_mov_b32_e32 v114, v3
	v_lshlrev_b32_e32 v104, 2, v0
	v_lshlrev_b64 v[102:103], 22, v[102:103]
	v_lshlrev_b32_e32 v118, 6, v0
	v_lshlrev_b32_e32 v0, 7, v0
	v_and_b32_e32 v104, 0x7c0, v104
	v_lshl_add_u64 v[102:103], s[12:13], 0, v[102:103]
	v_cndmask_b32_e32 v117, 0, v41, vcc
	v_and_b32_e32 v0, 0x700, v0
	v_and_b32_e32 v118, 64, v118
	v_or3_b32 v0, v118, v117, v0
	s_waitcnt lgkmcnt(0)
	v_mov_b32_e32 v16, s78
	v_mov_b32_e32 v17, s79
	v_lshl_add_u64 v[16:17], v[16:17], 0, v[18:19]
	v_lshl_add_u64 v[16:17], v[16:17], 0, v[2:3]
	v_lshlrev_b32_e32 v2, 14, v42
	v_lshl_add_u64 v[16:17], v[16:17], 0, v[14:15]
	v_lshl_add_u64 v[86:87], v[16:17], 0, v[2:3]
	v_add_co_u32_e64 v46, s[4:5], s44, v86
	global_load_dwordx4 v[16:19], v[86:87], off nt
	s_nop 0
	v_addc_co_u32_e64 v47, s[4:5], 0, v87, s[4:5]
	v_add_co_u32_e64 v50, s[4:5], s62, v86
	v_mov_b32_e32 v2, v3
	s_nop 0
	v_addc_co_u32_e64 v51, s[4:5], 0, v87, s[4:5]
	v_add_co_u32_e64 v58, s[4:5], s63, v86
	global_load_dwordx4 v[42:45], v[46:47], off offset:-4096 nt
	s_nop 0
	global_load_dwordx4 v[46:49], v[46:47], off nt
	s_nop 0
	global_load_dwordx4 v[50:53], v[50:51], off nt
	v_addc_co_u32_e64 v59, s[4:5], 0, v87, s[4:5]
	v_add_co_u32_e64 v66, s[4:5], s64, v86
	s_nop 1
	v_addc_co_u32_e64 v67, s[4:5], 0, v87, s[4:5]
	v_add_co_u32_e64 v74, s[4:5], s65, v86
	global_load_dwordx4 v[54:57], v[58:59], off offset:-4096 nt
	s_nop 0
	global_load_dwordx4 v[58:61], v[58:59], off nt
	s_nop 0
	global_load_dwordx4 v[62:65], v[66:67], off offset:-4096 nt
	s_nop 0
	global_load_dwordx4 v[66:69], v[66:67], off nt
	v_addc_co_u32_e64 v75, s[4:5], 0, v87, s[4:5]
	v_add_co_u32_e64 v82, s[4:5], s71, v86
	s_nop 1
	v_addc_co_u32_e64 v83, s[4:5], 0, v87, s[4:5]
	v_add_co_u32_e64 v90, s[4:5], s72, v86
	global_load_dwordx4 v[70:73], v[74:75], off offset:-4096 nt
	s_nop 0
	global_load_dwordx4 v[74:77], v[74:75], off nt
	s_nop 0
	global_load_dwordx4 v[78:81], v[82:83], off offset:-4096 nt
	s_nop 0
	global_load_dwordx4 v[82:85], v[82:83], off nt
	v_addc_co_u32_e64 v91, s[4:5], 0, v87, s[4:5]
	v_add_co_u32_e64 v98, s[4:5], s73, v86
	s_nop 0
	s_nop 0
	v_addc_co_u32_e64 v99, s[4:5], 0, v87, s[4:5]
	global_load_dwordx4 v[86:89], v[90:91], off offset:-4096 nt
	s_nop 0
	global_load_dwordx4 v[90:93], v[90:91], off nt
	s_nop 0
	global_load_dwordx4 v[94:97], v[98:99], off offset:-4096 nt
	s_nop 0
	global_load_dwordx4 v[98:101], v[98:99], off nt
	s_waitcnt vmcnt(15)
	v_mul_f32_e32 v16, 0x43800000, v16
	s_waitcnt vmcnt(14)
	v_mul_f32_e32 v42, 0x43800000, v42
	v_mul_f32_e32 v17, 0x43800000, v17
	v_mul_f32_e32 v43, 0x43800000, v43
	v_cvt_pk_fp8_f32 v2, v16, v42
	v_mul_f32_e32 v18, 0x43800000, v18
	v_mul_f32_e32 v44, 0x43800000, v44
	v_cvt_pk_fp8_f32 v15, v17, v43
	v_mul_f32_e32 v19, 0x43800000, v19
	v_mul_f32_e32 v45, 0x43800000, v45
	v_cvt_pk_fp8_f32 v105, v18, v44
	s_waitcnt vmcnt(13)
	v_mul_f32_e32 v46, 0x43800000, v46
	s_waitcnt vmcnt(12)
	v_mul_f32_e32 v50, 0x43800000, v50
	v_cvt_pk_fp8_f32 v106, v19, v45
	v_mul_f32_e32 v47, 0x43800000, v47
	v_mul_f32_e32 v51, 0x43800000, v51
	v_cvt_pk_fp8_f32 v2, v46, v50 op_sel:[0,0,1]
	v_mul_f32_e32 v48, 0x43800000, v48
	v_mul_f32_e32 v52, 0x43800000, v52
	v_cvt_pk_fp8_f32 v15, v47, v51 op_sel:[0,0,1]
	v_mul_f32_e32 v49, 0x43800000, v49
	v_mul_f32_e32 v53, 0x43800000, v53
	v_cvt_pk_fp8_f32 v105, v48, v52 op_sel:[0,0,1]
	v_cvt_pk_fp8_f32 v106, v49, v53 op_sel:[0,0,1]
	v_mov_b32_e32 v18, v3
	v_mov_b32_e32 v19, v3
	s_waitcnt vmcnt(11)
	v_mul_f32_e32 v54, 0x43800000, v54
	s_waitcnt vmcnt(10)
; #define LAS __attribute__((address_space(3)))
; __device__ __forceinline__ unsigned pk4_fp8(float a, float b, float c, float d) { unsigned w = 0u; w = __builtin_amdgcn_cvt_pk_fp8_f32(a, b, w, false); w = __builtin_amdgcn_cvt_pk_fp8_f32(c, d, w, true); return w; }
; __device__ __forceinline__ void conv_item8(const float* W, int K, int N, unsigned char* WT, int k0, int n0, int drow0, LAS unsigned* scr, int lane, float sc, bool rperm = false) {
;     ...
; #pragma unroll
;     for (int i = 0; i < 4; ++i) { const int rp = 4 * i + q; LAS unsigned* sp = scr + (4 * n4) * 17 + rp;
;         sp[0]  = pk4_fp8(v[i][0].x * sc, v[i][1].x * sc, v[i][2].x * sc, v[i][3].x * sc);
;         sp[17] = pk4_fp8(v[i][0].y * sc, v[i][1].y * sc, v[i][2].y * sc, v[i][3].y * sc);
;         sp[34] = pk4_fp8(v[i][0].z * sc, v[i][1].z * sc, v[i][2].z * sc, v[i][3].z * sc);
;         sp[51] = pk4_fp8(v[i][0].w * sc, v[i][1].w * sc, v[i][2].w * sc, v[i][3].w * sc); }
;     asm volatile("s_waitcnt lgkmcnt(0)" ::: "memory");
;     const int c = lane & 3;
; #pragma unroll
;     for (int j = 0; j < 4; ++j) {
;         const int n = (lane >> 2) + 16 * j; const LAS unsigned* sp = scr + n * 17 + 4 * c;
;         u32x4 o; o.x = sp[0]; o.y = sp[1]; o.z = sp[2]; o.w = sp[3];
;         const int nr = (rperm && n < 32) ? ((n < 16) ? 2 * n : 2 * (n - 16) + 1) : n;
;         *(u32x4*)(WT + (size_t)(drow0 + nr) * K + k0 + 16 * c) = o;
;     }
;     asm volatile("s_waitcnt lgkmcnt(0)" ::: "memory");
	v_mul_f32_e32 v58, 0x43800000, v58
	v_mul_f32_e32 v55, 0x43800000, v55
	v_mul_f32_e32 v59, 0x43800000, v59
	v_cvt_pk_fp8_f32 v107, v54, v58
	v_mul_f32_e32 v56, 0x43800000, v56
	v_mul_f32_e32 v60, 0x43800000, v60
	v_cvt_pk_fp8_f32 v108, v55, v59
	v_mul_f32_e32 v57, 0x43800000, v57
	v_mul_f32_e32 v61, 0x43800000, v61
	v_cvt_pk_fp8_f32 v109, v56, v60
	s_waitcnt vmcnt(9)
	v_mul_f32_e32 v62, 0x43800000, v62
	s_waitcnt vmcnt(8)
	v_mul_f32_e32 v66, 0x43800000, v66
	v_cvt_pk_fp8_f32 v110, v57, v61
	v_mul_f32_e32 v63, 0x43800000, v63
	v_mul_f32_e32 v67, 0x43800000, v67
	v_cvt_pk_fp8_f32 v107, v62, v66 op_sel:[0,0,1]
	v_mul_f32_e32 v64, 0x43800000, v64
	v_mul_f32_e32 v68, 0x43800000, v68
	v_cvt_pk_fp8_f32 v108, v63, v67 op_sel:[0,0,1]
	v_mul_f32_e32 v65, 0x43800000, v65
	v_mul_f32_e32 v69, 0x43800000, v69
	s_waitcnt vmcnt(7)
	v_mul_f32_e32 v70, 0x43800000, v70
	s_waitcnt vmcnt(6)
	v_mul_f32_e32 v74, 0x43800000, v74
	s_waitcnt vmcnt(3)
	v_mul_f32_e32 v86, 0x43800000, v86
	s_waitcnt vmcnt(2)
	v_mul_f32_e32 v90, 0x43800000, v90
	v_cvt_pk_fp8_f32 v109, v64, v68 op_sel:[0,0,1]
	v_mul_f32_e32 v71, 0x43800000, v71
	v_mul_f32_e32 v75, 0x43800000, v75
	v_mul_f32_e32 v87, 0x43800000, v87
	v_mul_f32_e32 v91, 0x43800000, v91
	v_cvt_pk_fp8_f32 v111, v70, v74
	v_cvt_pk_fp8_f32 v115, v86, v90
	v_cvt_pk_fp8_f32 v110, v65, v69 op_sel:[0,0,1]
	v_mul_f32_e32 v72, 0x43800000, v72
	v_mul_f32_e32 v76, 0x43800000, v76
	v_cvt_pk_fp8_f32 v112, v71, v75
	v_cvt_pk_fp8_f32 v116, v87, v91
	ds_write2_b32 v22, v2, v107 offset1:4
	ds_write2_b32 v22, v15, v108 offset0:17 offset1:21
	ds_write2_b32 v22, v105, v109 offset0:34 offset1:38
	ds_write2_b32 v22, v106, v110 offset0:51 offset1:55
	v_mul_f32_e32 v2, 0x43800000, v88
	v_mul_f32_e32 v15, 0x43800000, v92
	v_mul_f32_e32 v73, 0x43800000, v73
	v_mul_f32_e32 v77, 0x43800000, v77
	v_cvt_pk_fp8_f32 v113, v72, v76
	v_cvt_pk_fp8_f32 v18, v2, v15
	v_mul_f32_e32 v2, 0x43800000, v89
	v_mul_f32_e32 v15, 0x43800000, v93
	v_mul_f32_e32 v78, 0x43800000, v78
	v_mul_f32_e32 v82, 0x43800000, v82
	s_waitcnt vmcnt(1)
	v_mul_f32_e32 v94, 0x43800000, v94
	s_waitcnt vmcnt(0)
	v_mul_f32_e32 v98, 0x43800000, v98
	v_cvt_pk_fp8_f32 v114, v73, v77
	v_cvt_pk_fp8_f32 v19, v2, v15
	v_mul_f32_e32 v79, 0x43800000, v79
	v_mul_f32_e32 v83, 0x43800000, v83
	v_mul_f32_e32 v95, 0x43800000, v95
	v_mul_f32_e32 v99, 0x43800000, v99
	v_cvt_pk_fp8_f32 v111, v78, v82 op_sel:[0,0,1]
	v_cvt_pk_fp8_f32 v115, v94, v98 op_sel:[0,0,1]
	v_mul_f32_e32 v80, 0x43800000, v80
	v_mul_f32_e32 v84, 0x43800000, v84
	v_cvt_pk_fp8_f32 v112, v79, v83 op_sel:[0,0,1]
	v_cvt_pk_fp8_f32 v116, v95, v99 op_sel:[0,0,1]
	v_mul_f32_e32 v16, 0x43800000, v96
	v_mul_f32_e32 v17, 0x43800000, v100
	v_mul_f32_e32 v81, 0x43800000, v81
	v_mul_f32_e32 v85, 0x43800000, v85
	v_cvt_pk_fp8_f32 v113, v80, v84 op_sel:[0,0,1]
	v_cvt_pk_fp8_f32 v18, v16, v17 op_sel:[0,0,1]
	v_mul_f32_e32 v2, 0x43800000, v97
	v_mul_f32_e32 v15, 0x43800000, v101
	v_cvt_pk_fp8_f32 v114, v81, v85 op_sel:[0,0,1]
	v_cvt_pk_fp8_f32 v19, v2, v15 op_sel:[0,0,1]
	ds_write2_b32 v22, v111, v115 offset0:8 offset1:12
	ds_write2_b32 v22, v112, v116 offset0:25 offset1:29
	ds_write2_b32 v22, v113, v18 offset0:42 offset1:46
	ds_write2_b32 v22, v114, v19 offset0:59 offset1:63
	v_mov_b32_e32 v105, v3
	s_waitcnt lgkmcnt(0)
	v_lshl_add_u64 v[16:17], v[102:103], 0, v[104:105]
	v_lshl_add_u64 v[46:47], v[16:17], 0, v[4:5]
	ds_read2_b32 v[16:17], v30 offset1:1
	ds_read2_b32 v[18:19], v30 offset0:2 offset1:3
	v_or_b32_e32 v2, v0, v23
	ds_read2_b32 v[42:43], v31 offset1:1
	ds_read2_b32 v[44:45], v32 offset1:1
	v_lshlrev_b32_e32 v2, 11, v2
	v_lshl_add_u64 v[48:49], v[46:47], 0, v[2:3]
	v_or_b32_e32 v2, v0, v24
	v_lshlrev_b32_e32 v2, 11, v2
	s_waitcnt lgkmcnt(2)
	global_store_dwordx4 v[48:49], v[16:19], off
	s_nop 1
	v_lshl_add_u64 v[16:17], v[46:47], 0, v[2:3]
	s_waitcnt lgkmcnt(0)
	global_store_dwordx4 v[16:17], v[42:45], off
	ds_read2_b32 v[16:17], v33 offset1:1
	ds_read2_b32 v[18:19], v34 offset1:1
	ds_read2_b32 v[42:43], v35 offset1:1
	ds_read2_b32 v[44:45], v36 offset1:1
	v_or_b32_e32 v2, v0, v25
	v_lshlrev_b32_e32 v2, 11, v2
	v_or_b32_e32 v0, v0, v26
	v_lshl_add_u64 v[48:49], v[46:47], 0, v[2:3]
	v_lshlrev_b32_e32 v2, 11, v0
	s_waitcnt lgkmcnt(2)
	global_store_dwordx4 v[48:49], v[16:19], off
	s_nop 1
	v_lshl_add_u64 v[16:17], v[46:47], 0, v[2:3]
	s_waitcnt lgkmcnt(0)
	global_store_dwordx4 v[16:17], v[42:45], off
	s_waitcnt lgkmcnt(0)

; __device__ __forceinline__ void conv_item8(const float* W, int K, int N, unsigned char* WT, int k0, int n0, int drow0, LAS unsigned* scr, int lane, float sc, bool rperm = false) {
;     const int q = lane >> 4, n4 = lane & 15;
;     f32x4 v[4][4];
; #pragma unroll
;     for (int i = 0; i < 4; ++i)
; #pragma unroll
;         for (int t = 0; t < 4; ++t) v[i][t] = __builtin_nontemporal_load((const f32x4*)(W + (size_t)(k0 + 4 * (4 * i + q) + t) * N + n0 + 4 * n4));
; #pragma unroll
;     for (int i = 0; i < 4; ++i) { const int rp = 4 * i + q; LAS unsigned* sp = scr + (4 * n4) * 17 + rp;
;         sp[0]  = pk4_fp8(v[i][0].x * sc, v[i][1].x * sc, v[i][2].x * sc, v[i][3].x * sc);
;         sp[17] = pk4_fp8(v[i][0].y * sc, v[i][1].y * sc, v[i][2].y * sc, v[i][3].y * sc);
;         sp[34] = pk4_fp8(v[i][0].z * sc, v[i][1].z * sc, v[i][2].z * sc, v[i][3].z * sc);
; __device__ __forceinline__ void conv_dispatch(const Params& p, int it, LAS unsigned* scr, int lane) {
;     ...
;     int r = it; const int l = (r >= I_L0) ? 1 : 0; if (l) r -= I_L0;
;     const int i_in = l ? I_IN1 : I_IN0;
;     if (r < i_in) { const int N = l ? ODW : EVW, nb = N / 64;
;         conv_item8(p.in[l ? 16 : 5], D, N, l ? p.wp[IX_WIN1] : p.wp[IX_WIN0], (r / nb) * 64, (r % nb) * 64, (r % nb) * 64, scr, lane, F8_SW, l == 1 && (r % nb) < 64 && ((r % nb) & 1) == 0);
;         return; } r -= i_in;
;     if (r < I_OUT) { if (OUT_F8) conv_item8(p.in[l ? 19 : 8], D, D, l ? p.wp[IX_WOUT1] : p.wp[IX_WOUT0], (r / 32) * 64, (r % 32) * 64, (r % 32) * 64, scr, lane, F8_SWD);
;         else conv_item(p.in[l ? 19 : 8], D, D, (bf16_t*)(l ? p.wp[IX_WOUT1] : p.wp[IX_WOUT0]), (r / 32) * 64, (r % 32) * 64, (r % 32) * 64, scr, lane); return; } r -= I_OUT;
;     if (r < 2 * I_G) { const int up = r >= I_G; if (up) r -= I_G; const int e = r / 512, rr = r % 512, kb = rr / 16, nb = rr % 16, n0 = nb * 64;
;         conv_item8(p.in[(l ? 21 : 10) + up] + (size_t)e * D * DFF, D, DFF, (l ? p.wp[IX_WGU1] : p.wp[IX_WGU0]) + (size_t)e * 2048 * D, kb * 64, n0, (n0 >> 7) * 256 + (n0 & 127) + up * 128, scr, lane, F8_SW);
;         return; } r -= 2 * I_G;
;     { const int e = r / 512, rr = r % 512, kb = rr / 32, nb = rr % 32;
;         conv_item8(p.in[l ? 23 : 12] + (size_t)e * DFF * D, DFF, D, (l ? p.wp[IX_WD1] : p.wp[IX_WD0]) + (size_t)e * D * DFF, kb * 64, nb * 64, nb * 64, scr, lane, F8_SWD); }
.LBB0_920:
	s_movk_i32 s6, 0x73ff
	v_add_u32_e32 v4, 0xffff8c00, v78
	v_cmp_lt_i32_e32 vcc, s6, v78
	v_mov_b32_e32 v2, 0x1000
	v_mov_b32_e32 v5, 0xc00
	v_cndmask_b32_e32 v2, v2, v5, vcc
	v_cndmask_b32_e32 v4, v78, v4, vcc
	v_cmp_ge_i32_e64 s[6:7], v4, v2
	s_and_saveexec_b64 s[8:9], s[6:7]
	s_xor_b64 s[8:9], exec, s[8:9]
	s_cbranch_execz .LBB0_930
	v_sub_u32_e32 v5, v4, v2
	s_movk_i32 s6, 0x3ff
	v_cmp_lt_i32_e64 s[6:7], s6, v5
	s_and_saveexec_b64 s[86:87], s[6:7]
	s_xor_b64 s[86:87], exec, s[86:87]
	s_cbranch_execz .LBB0_927
	s_movk_i32 s6, 0x43ff
	v_cmp_lt_u32_e64 s[6:7], s6, v5
	s_and_saveexec_b64 s[88:89], s[6:7]
	s_xor_b64 s[88:89], exec, s[88:89]
	s_cbranch_execz .LBB0_924
	v_add_u32_e32 v2, 0xffffbc00, v5
	v_lshrrev_b32_e32 v6, 9, v2
	v_mov_b32_e32 v2, 0x60
	v_mov_b32_e32 v5, 0xb8
	v_cndmask_b32_e32 v2, v2, v5, vcc
	v_lshl_add_u64 v[8:9], s[0:1], 0, v[2:3]
	s_nop 0
	v_readfirstlane_b32 s98, v8
	v_readfirstlane_b32 s99, v9
	s_nop 4
	s_load_dwordx2 s[100:101], s[98:99], 0x0
	v_mov_b32_e32 v7, v3
	v_lshlrev_b64 v[10:11], 23, v[6:7]
	v_mov_b32_e32 v2, s37
	v_mov_b32_e32 v5, s39
	v_mov_b32_e32 v71, v3
	v_lshlrev_b64 v[6:7], 21, v[6:7]
	v_mov_b32_e32 v75, v3
	s_waitcnt lgkmcnt(0)
	v_mov_b32_e32 v8, s100
	v_mov_b32_e32 v9, s101
	v_lshl_add_u64 v[8:9], v[8:9], 0, v[10:11]
	v_cndmask_b32_e32 v11, v2, v5, vcc
	v_mov_b32_e32 v2, s36
	v_mov_b32_e32 v5, s38
	v_cndmask_b32_e32 v10, v2, v5, vcc
	v_lshlrev_b32_e32 v2, 1, v4
	v_and_b32_e32 v74, 0x3c0, v2
	v_lshlrev_b32_e32 v2, 6, v4
	v_and_b32_e32 v76, 0x7c0, v2
	v_lshlrev_b32_e32 v2, 2, v76
	v_lshl_add_u64 v[4:5], v[8:9], 0, v[2:3]
	v_lshl_add_u64 v[4:5], v[4:5], 0, v[70:71]
	v_lshl_or_b32 v2, v74, 13, v87
	v_lshl_add_u64 v[20:21], v[4:5], 0, v[2:3]
	v_add_co_u32_e64 v4, s[6:7], s77, v20
	global_load_dwordx4 v[48:51], v[20:21], off nt
	s_nop 0
	v_addc_co_u32_e64 v5, s[6:7], 0, v21, s[6:7]
	s_movk_i32 s6, 0x4000
	global_load_dwordx4 v[52:55], v[4:5], off nt
	v_add_co_u32_e64 v4, s[6:7], s6, v20
	v_lshl_add_u64 v[72:73], v[10:11], 0, v[6:7]
	s_nop 0
	v_addc_co_u32_e64 v5, s[6:7], 0, v21, s[6:7]
	s_movk_i32 s6, 0x6000
	global_load_dwordx4 v[60:63], v[4:5], off nt
	v_add_co_u32_e64 v4, s[6:7], s6, v20
	s_nop 1
	v_addc_co_u32_e64 v5, s[6:7], 0, v21, s[6:7]
	s_mov_b32 s6, 0x20000
	global_load_dwordx4 v[64:67], v[4:5], off nt
	v_add_co_u32_e64 v4, s[6:7], s6, v20
	s_nop 1
	v_addc_co_u32_e64 v5, s[6:7], 0, v21, s[6:7]
	s_mov_b32 s6, 0x22000
	global_load_dwordx4 v[36:39], v[4:5], off nt
	v_add_co_u32_e64 v4, s[6:7], s6, v20
	s_nop 1
	v_addc_co_u32_e64 v5, s[6:7], 0, v21, s[6:7]
	s_mov_b32 s6, 0x24000
	global_load_dwordx4 v[40:43], v[4:5], off nt
	v_add_co_u32_e64 v4, s[6:7], s6, v20
	s_nop 1
	v_addc_co_u32_e64 v5, s[6:7], 0, v21, s[6:7]
	s_mov_b32 s6, 0x26000
	global_load_dwordx4 v[44:47], v[4:5], off nt
	v_add_co_u32_e64 v4, s[6:7], s6, v20
	s_nop 0
	s_nop 0
	v_addc_co_u32_e64 v5, s[6:7], 0, v21, s[6:7]
	s_mov_b32 s6, 0x40000
	global_load_dwordx4 v[56:59], v[4:5], off nt
	v_add_co_u32_e64 v4, s[6:7], s6, v20
	s_nop 0
	s_nop 0
	v_addc_co_u32_e64 v5, s[6:7], 0, v21, s[6:7]
	s_mov_b32 s6, 0x42000
	global_load_dwordx4 v[12:15], v[4:5], off nt
	v_add_co_u32_e64 v4, s[6:7], s6, v20
	s_nop 0
	s_nop 0
	v_addc_co_u32_e64 v5, s[6:7], 0, v21, s[6:7]
	s_mov_b32 s6, 0x44000
	global_load_dwordx4 v[24:27], v[4:5], off nt
	v_add_co_u32_e64 v4, s[6:7], s6, v20
	s_nop 0
	s_nop 0
	v_addc_co_u32_e64 v5, s[6:7], 0, v21, s[6:7]
	s_mov_b32 s6, 0x46000
	global_load_dwordx4 v[28:31], v[4:5], off nt
	v_add_co_u32_e64 v4, s[6:7], s6, v20
	s_nop 0
	s_nop 0
	v_addc_co_u32_e64 v5, s[6:7], 0, v21, s[6:7]
	global_load_dwordx4 v[32:35], v[4:5], off nt
	s_mov_b32 s6, 0x60000
	v_add_co_u32_e64 v4, s[6:7], s6, v20
	s_nop 0
	s_nop 0
	v_addc_co_u32_e64 v5, s[6:7], 0, v21, s[6:7]
	s_mov_b32 s6, 0x62000
	s_nop 0
	v_add_co_u32_e64 v8, s[6:7], s6, v20
	global_load_dwordx4 v[4:7], v[4:5], off nt
	s_nop 0
	v_addc_co_u32_e64 v9, s[6:7], 0, v21, s[6:7]
	s_mov_b32 s6, 0x64000
	s_nop 0
	v_add_co_u32_e64 v16, s[6:7], s6, v20
	global_load_dwordx4 v[8:11], v[8:9], off nt
	s_nop 0
	v_addc_co_u32_e64 v17, s[6:7], 0, v21, s[6:7]
	s_mov_b32 s6, 0x66000
	s_nop 0
	v_add_co_u32_e64 v20, s[6:7], s6, v20
	global_load_dwordx4 v[16:19], v[16:17], off nt
	s_nop 0
	v_addc_co_u32_e64 v21, s[6:7], 0, v21, s[6:7]
	global_load_dwordx4 v[20:23], v[20:21], off nt
	s_waitcnt vmcnt(15)
	v_mul_f32_e32 v2, 0x43800000, v48
	s_waitcnt vmcnt(14)
	v_mul_f32_e32 v48, 0x43800000, v52
	s_waitcnt vmcnt(13)
	v_mul_f32_e32 v52, 0x43800000, v60
	s_waitcnt vmcnt(12)
	v_mul_f32_e32 v60, 0x43800000, v64
	v_mov_b32_e32 v64, v3
	v_cvt_pk_fp8_f32 v64, v2, v48
	v_mul_f32_e32 v2, 0x43800000, v49
	v_mul_f32_e32 v48, 0x43800000, v53
	v_mov_b32_e32 v53, v3
	v_cvt_pk_fp8_f32 v53, v2, v48
	v_cvt_pk_fp8_f32 v64, v52, v60 op_sel:[0,0,1]
	v_mul_f32_e32 v49, 0x43800000, v61
	v_mul_f32_e32 v52, 0x43800000, v65
	v_cvt_pk_fp8_f32 v53, v49, v52 op_sel:[0,0,1]
	v_mul_f32_e32 v2, 0x43800000, v50
	v_mul_f32_e32 v48, 0x43800000, v54
	v_mov_b32_e32 v52, v3
	v_cvt_pk_fp8_f32 v52, v2, v48
	v_mul_f32_e32 v2, 0x43800000, v51
	v_mul_f32_e32 v48, 0x43800000, v55
	v_mov_b32_e32 v51, v3
	v_cvt_pk_fp8_f32 v51, v2, v48
	s_waitcnt vmcnt(11)
	v_mul_f32_e32 v2, 0x43800000, v36
	s_waitcnt vmcnt(10)
	v_mul_f32_e32 v36, 0x43800000, v40
	v_mov_b32_e32 v48, v3
	v_cvt_pk_fp8_f32 v48, v2, v36
	v_mul_f32_e32 v2, 0x43800000, v37
	v_mul_f32_e32 v36, 0x43800000, v41
	v_mov_b32_e32 v41, v3
	v_cvt_pk_fp8_f32 v41, v2, v36
	s_waitcnt vmcnt(9)
	v_mul_f32_e32 v40, 0x43800000, v44
	v_mul_f32_e32 v37, 0x43800000, v45
	v_mul_f32_e32 v2, 0x43800000, v38
	v_mul_f32_e32 v36, 0x43800000, v42
	v_mul_f32_e32 v49, 0x43800000, v62
	v_mul_f32_e32 v50, 0x43800000, v66
	v_cvt_pk_fp8_f32 v52, v49, v50 op_sel:[0,0,1]
	s_waitcnt vmcnt(8)
; #define LAS __attribute__((address_space(3)))
; __device__ __forceinline__ unsigned pk4_fp8(float a, float b, float c, float d) { unsigned w = 0u; w = __builtin_amdgcn_cvt_pk_fp8_f32(a, b, w, false); w = __builtin_amdgcn_cvt_pk_fp8_f32(c, d, w, true); return w; }
; __device__ __forceinline__ void conv_item8(const float* W, int K, int N, unsigned char* WT, int k0, int n0, int drow0, LAS unsigned* scr, int lane, float sc, bool rperm = false) {
;     ...
; #pragma unroll
;     for (int i = 0; i < 4; ++i) { const int rp = 4 * i + q; LAS unsigned* sp = scr + (4 * n4) * 17 + rp;
;         sp[0]  = pk4_fp8(v[i][0].x * sc, v[i][1].x * sc, v[i][2].x * sc, v[i][3].x * sc);
;         sp[17] = pk4_fp8(v[i][0].y * sc, v[i][1].y * sc, v[i][2].y * sc, v[i][3].y * sc);
;         sp[34] = pk4_fp8(v[i][0].z * sc, v[i][1].z * sc, v[i][2].z * sc, v[i][3].z * sc);
;         sp[51] = pk4_fp8(v[i][0].w * sc, v[i][1].w * sc, v[i][2].w * sc, v[i][3].w * sc); }
;     asm volatile("s_waitcnt lgkmcnt(0)" ::: "memory");
;     const int c = lane & 3;
; #pragma unroll
;     for (int j = 0; j < 4; ++j) {
;         const int n = (lane >> 2) + 16 * j; const LAS unsigned* sp = scr + n * 17 + 4 * c;
;         u32x4 o; o.x = sp[0]; o.y = sp[1]; o.z = sp[2]; o.w = sp[3];
;         const int nr = (rperm && n < 32) ? ((n < 16) ? 2 * n : 2 * (n - 16) + 1) : n;
;         *(u32x4*)(WT + (size_t)(drow0 + nr) * K + k0 + 16 * c) = o;
;     }
;     asm volatile("s_waitcnt lgkmcnt(0)" ::: "memory");
	v_mul_f32_e32 v44, 0x43800000, v56
	v_cvt_pk_fp8_f32 v48, v40, v44 op_sel:[0,0,1]
	v_mul_f32_e32 v40, 0x43800000, v57
	v_cvt_pk_fp8_f32 v41, v37, v40 op_sel:[0,0,1]
	v_mov_b32_e32 v40, v3
	v_cvt_pk_fp8_f32 v40, v2, v36
	v_mul_f32_e32 v2, 0x43800000, v39
	v_mul_f32_e32 v36, 0x43800000, v43
	v_mov_b32_e32 v39, v3
	v_cvt_pk_fp8_f32 v39, v2, v36
	s_waitcnt vmcnt(7)
	v_mul_f32_e32 v2, 0x43800000, v12
	v_mul_f32_e32 v37, 0x43800000, v46
	v_mul_f32_e32 v38, 0x43800000, v58
	v_mul_f32_e32 v49, 0x43800000, v63
	s_waitcnt vmcnt(6)
	v_mul_f32_e32 v12, 0x43800000, v24
	v_mul_f32_e32 v50, 0x43800000, v67
	v_cvt_pk_fp8_f32 v40, v37, v38 op_sel:[0,0,1]
	v_mul_f32_e32 v37, 0x43800000, v47
	v_mul_f32_e32 v38, 0x43800000, v59
	v_cvt_pk_fp8_f32 v51, v49, v50 op_sel:[0,0,1]
	v_cvt_pk_fp8_f32 v39, v37, v38 op_sel:[0,0,1]
	s_waitcnt vmcnt(5)
	v_mul_f32_e32 v24, 0x43800000, v28
	ds_write2_b32 v81, v64, v48 offset1:4
	ds_write2_b32 v81, v53, v41 offset0:17 offset1:21
	ds_write2_b32 v81, v52, v40 offset0:34 offset1:38
	ds_write2_b32 v81, v51, v39 offset0:51 offset1:55
	s_waitcnt vmcnt(4)
	v_mul_f32_e32 v28, 0x43800000, v32
	v_mov_b32_e32 v32, v3
	v_cvt_pk_fp8_f32 v32, v2, v12
	v_mul_f32_e32 v2, 0x43800000, v13
	v_mul_f32_e32 v12, 0x43800000, v25
	v_mov_b32_e32 v25, v3
	v_cvt_pk_fp8_f32 v25, v2, v12
	v_cvt_pk_fp8_f32 v32, v24, v28 op_sel:[0,0,1]
	v_mul_f32_e32 v13, 0x43800000, v29
	v_mul_f32_e32 v24, 0x43800000, v33
	v_cvt_pk_fp8_f32 v25, v13, v24 op_sel:[0,0,1]
	v_mul_f32_e32 v2, 0x43800000, v14
	v_mul_f32_e32 v12, 0x43800000, v26
	v_mov_b32_e32 v24, v3
	v_cvt_pk_fp8_f32 v24, v2, v12
	v_mul_f32_e32 v2, 0x43800000, v15
	v_mul_f32_e32 v12, 0x43800000, v27
	v_mov_b32_e32 v15, v3
	v_cvt_pk_fp8_f32 v15, v2, v12
	v_mul_f32_e32 v13, 0x43800000, v30
	v_mul_f32_e32 v14, 0x43800000, v34
	v_cvt_pk_fp8_f32 v24, v13, v14 op_sel:[0,0,1]
	v_mul_f32_e32 v13, 0x43800000, v31
	v_mul_f32_e32 v14, 0x43800000, v35
	v_cvt_pk_fp8_f32 v15, v13, v14 op_sel:[0,0,1]
	s_waitcnt vmcnt(3)
	v_mul_f32_e32 v2, 0x43800000, v4
	s_waitcnt vmcnt(2)
	v_mul_f32_e32 v4, 0x43800000, v8
	v_mov_b32_e32 v13, v3
	v_cvt_pk_fp8_f32 v13, v2, v4
	v_mul_f32_e32 v2, 0x43800000, v5
	v_mul_f32_e32 v4, 0x43800000, v9
	v_mov_b32_e32 v9, v3
	v_cvt_pk_fp8_f32 v9, v2, v4
	s_waitcnt vmcnt(1)
	v_mul_f32_e32 v8, 0x43800000, v16
	s_waitcnt vmcnt(0)
	v_mul_f32_e32 v12, 0x43800000, v20
	v_cvt_pk_fp8_f32 v13, v8, v12 op_sel:[0,0,1]
	v_mul_f32_e32 v5, 0x43800000, v17
	v_mul_f32_e32 v8, 0x43800000, v21
	v_cvt_pk_fp8_f32 v9, v5, v8 op_sel:[0,0,1]
	v_mul_f32_e32 v2, 0x43800000, v6
	v_mul_f32_e32 v4, 0x43800000, v10
	v_mov_b32_e32 v8, v3
	v_cvt_pk_fp8_f32 v8, v2, v4
	v_mul_f32_e32 v2, 0x43800000, v7
	v_mul_f32_e32 v4, 0x43800000, v11
	v_mov_b32_e32 v7, v3
	v_cvt_pk_fp8_f32 v7, v2, v4
	v_mul_f32_e32 v5, 0x43800000, v18
	v_mul_f32_e32 v6, 0x43800000, v22
	v_cvt_pk_fp8_f32 v8, v5, v6 op_sel:[0,0,1]
	v_mul_f32_e32 v5, 0x43800000, v19
	v_mul_f32_e32 v6, 0x43800000, v23
	v_cvt_pk_fp8_f32 v7, v5, v6 op_sel:[0,0,1]
	ds_write2_b32 v81, v32, v13 offset0:8 offset1:12
	ds_write2_b32 v81, v25, v9 offset0:25 offset1:29
	ds_write2_b32 v81, v24, v8 offset0:42 offset1:46
	ds_write2_b32 v81, v15, v7 offset0:59 offset1:63
	s_waitcnt lgkmcnt(0)
	v_lshl_add_u64 v[4:5], v[72:73], 0, v[74:75]
	v_lshl_add_u64 v[8:9], v[4:5], 0, v[68:69]
	ds_read2_b32 v[4:5], v88 offset1:1
	ds_read2_b32 v[6:7], v88 offset0:2 offset1:3
	v_or_b32_e32 v2, v76, v82
	v_lshlrev_b32_e32 v2, 10, v2
	v_lshl_add_u64 v[10:11], v[8:9], 0, v[2:3]
	v_or_b32_e32 v2, v76, v83
	s_waitcnt lgkmcnt(0)
	global_store_dwordx4 v[10:11], v[4:7], off
	ds_read2_b32 v[4:5], v89 offset1:1
	ds_read2_b32 v[6:7], v90 offset1:1
	v_lshlrev_b32_e32 v2, 10, v2
	v_lshl_add_u64 v[10:11], v[8:9], 0, v[2:3]
	v_or_b32_e32 v2, v76, v84
	v_lshlrev_b32_e32 v2, 10, v2
	s_waitcnt lgkmcnt(0)
	global_store_dwordx4 v[10:11], v[4:7], off
	ds_read2_b32 v[4:5], v91 offset1:1
	ds_read2_b32 v[6:7], v92 offset1:1
	v_lshl_add_u64 v[10:11], v[8:9], 0, v[2:3]
	v_or_b32_e32 v2, v76, v85
	v_lshlrev_b32_e32 v2, 10, v2
	v_lshl_add_u64 v[8:9], v[8:9], 0, v[2:3]
	s_waitcnt lgkmcnt(0)
	global_store_dwordx4 v[10:11], v[4:7], off
	ds_read2_b32 v[4:5], v93 offset1:1
	ds_read2_b32 v[6:7], v94 offset1:1
	s_waitcnt lgkmcnt(0)
	global_store_dwordx4 v[8:9], v[4:7], off
	s_waitcnt lgkmcnt(0)
; #define LAS __attribute__((address_space(3)))
; __device__ __forceinline__ unsigned pk4_fp8(float a, float b, float c, float d) { unsigned w = 0u; w = __builtin_amdgcn_cvt_pk_fp8_f32(a, b, w, false); w = __builtin_amdgcn_cvt_pk_fp8_f32(c, d, w, true); return w; }
; __device__ __forceinline__ void conv_item8(const float* W, int K, int N, unsigned char* WT, int k0, int n0, int drow0, LAS unsigned* scr, int lane, float sc, bool rperm = false) {
;     const int q = lane >> 4, n4 = lane & 15;
;     f32x4 v[4][4];
; #pragma unroll
;     for (int i = 0; i < 4; ++i)
; #pragma unroll
;         for (int t = 0; t < 4; ++t) v[i][t] = __builtin_nontemporal_load((const f32x4*)(W + (size_t)(k0 + 4 * (4 * i + q) + t) * N + n0 + 4 * n4));
; #pragma unroll
;     for (int i = 0; i < 4; ++i) { const int rp = 4 * i + q; LAS unsigned* sp = scr + (4 * n4) * 17 + rp;
;         sp[0]  = pk4_fp8(v[i][0].x * sc, v[i][1].x * sc, v[i][2].x * sc, v[i][3].x * sc);
;         sp[17] = pk4_fp8(v[i][0].y * sc, v[i][1].y * sc, v[i][2].y * sc, v[i][3].y * sc);
;         sp[34] = pk4_fp8(v[i][0].z * sc, v[i][1].z * sc, v[i][2].z * sc, v[i][3].z * sc);
;         sp[51] = pk4_fp8(v[i][0].w * sc, v[i][1].w * sc, v[i][2].w * sc, v[i][3].w * sc); }
; __device__ __forceinline__ void conv_dispatch(const Params& p, int it, LAS unsigned* scr, int lane) {
;     ...
;     if (r < 2 * I_G) { const int up = r >= I_G; if (up) r -= I_G; const int e = r / 512, rr = r % 512, kb = rr / 16, nb = rr % 16, n0 = nb * 64;
;         conv_item8(p.in[(l ? 21 : 10) + up] + (size_t)e * D * DFF, D, DFF, (l ? p.wp[IX_WGU1] : p.wp[IX_WGU0]) + (size_t)e * 2048 * D, kb * 64, n0, (n0 >> 7) * 256 + (n0 & 127) + up * 128, scr, lane, F8_SW);
.LBB0_924:
	s_andn2_saveexec_b64 s[88:89], s[88:89]
	s_cbranch_execz .LBB0_926
	s_movk_i32 s6, 0x23ff
	v_cmp_lt_u32_e64 s[6:7], s6, v5
	v_mov_b32_e32 v0, 0xfffffc00
	v_mov_b32_e32 v1, 0xffffdc00
	v_cndmask_b32_e64 v2, v0, v1, s[6:7]
	v_mov_b32_e32 v0, 0x50
	v_mov_b32_e32 v1, 0xa8
	v_add_u32_e32 v5, v2, v5
	v_cndmask_b32_e32 v2, v0, v1, vcc
	v_lshl_add_u64 v[8:9], s[0:1], 0, v[2:3]
	v_cndmask_b32_e64 v2, 0, 1, s[6:7]
	v_lshlrev_b32_e32 v2, 3, v2
	v_lshl_add_u64 v[8:9], v[8:9], 0, v[2:3]
	s_nop 0
	v_readfirstlane_b32 s98, v8
	v_readfirstlane_b32 s99, v9
	s_nop 4
	s_load_dwordx2 s[100:101], s[98:99], 0x0
	v_lshrrev_b32_e32 v6, 9, v5
	v_mov_b32_e32 v7, v3
	v_lshlrev_b64 v[10:11], 23, v[6:7]
	v_mov_b32_e32 v2, s41
	v_lshlrev_b32_e32 v12, 6, v5
	v_lshlrev_b64 v[6:7], 22, v[6:7]
	v_mov_b32_e32 v71, v3
	v_mov_b32_e32 v75, v3
	s_waitcnt lgkmcnt(0)
	v_mov_b32_e32 v8, s100
	v_mov_b32_e32 v9, s101
	v_lshl_add_u64 v[8:9], v[8:9], 0, v[10:11]
	v_mov_b32_e32 v10, s43
	v_cndmask_b32_e32 v11, v2, v10, vcc
	v_mov_b32_e32 v2, s40
	v_mov_b32_e32 v10, s42
	v_cndmask_b32_e32 v10, v2, v10, vcc
	v_lshlrev_b32_e32 v2, 2, v5
	v_and_b32_e32 v74, 0x7c0, v2
	v_lshlrev_b32_e32 v2, 7, v5
	v_lshl_add_u64 v[72:73], v[10:11], 0, v[6:7]
	v_and_b32_e32 v2, 0x700, v2
	v_and_b32_e32 v6, 64, v12
	v_cndmask_b32_e64 v7, 0, v95, s[6:7]
	v_or3_b32 v76, v6, v7, v2
	v_lshlrev_b32_e32 v2, 8, v5
	s_movk_i32 s6, 0x1f0
	v_and_b32_e32 v2, 0xf00, v2
	v_and_or_b32 v6, v4, s6, v79
	v_lshl_add_u64 v[4:5], v[8:9], 0, v[2:3]
	v_lshl_add_u64 v[4:5], v[4:5], 0, v[70:71]
	v_lshlrev_b32_e32 v2, 14, v6
	v_lshl_add_u64 v[12:13], v[4:5], 0, v[2:3]
	v_add_co_u32_e64 v4, s[6:7], s77, v12
	global_load_dwordx4 v[52:55], v[12:13], off nt
	s_nop 0
	v_addc_co_u32_e64 v5, s[6:7], 0, v13, s[6:7]
	s_movk_i32 s6, 0x3000
	global_load_dwordx4 v[56:59], v[4:5], off offset:-4096 nt
	global_load_dwordx4 v[60:63], v[4:5], off nt
	v_add_co_u32_e64 v4, s[6:7], s6, v12
	s_nop 1
	v_addc_co_u32_e64 v5, s[6:7], 0, v13, s[6:7]
	global_load_dwordx4 v[64:67], v[4:5], off nt
	s_mov_b32 s6, 0x11000
	v_add_co_u32_e64 v4, s[6:7], s6, v12
	s_nop 1
	v_addc_co_u32_e64 v5, s[6:7], 0, v13, s[6:7]
	s_mov_b32 s6, 0x13000
	global_load_dwordx4 v[36:39], v[4:5], off offset:-4096 nt
	global_load_dwordx4 v[40:43], v[4:5], off nt
	v_add_co_u32_e64 v4, s[6:7], s6, v12
	s_nop 1
	v_addc_co_u32_e64 v5, s[6:7], 0, v13, s[6:7]
	global_load_dwordx4 v[44:47], v[4:5], off offset:-4096 nt
	global_load_dwordx4 v[48:51], v[4:5], off nt
	s_mov_b32 s6, 0x21000
	v_add_co_u32_e64 v4, s[6:7], s6, v12
	s_nop 1
	v_addc_co_u32_e64 v5, s[6:7], 0, v13, s[6:7]
	s_mov_b32 s6, 0x23000
	global_load_dwordx4 v[20:23], v[4:5], off offset:-4096 nt
	global_load_dwordx4 v[24:27], v[4:5], off nt
	v_add_co_u32_e64 v4, s[6:7], s6, v12
	s_nop 0
	s_nop 0
	v_addc_co_u32_e64 v5, s[6:7], 0, v13, s[6:7]
	global_load_dwordx4 v[28:31], v[4:5], off offset:-4096 nt
	global_load_dwordx4 v[32:35], v[4:5], off nt
	s_mov_b32 s6, 0x31000
	v_add_co_u32_e64 v8, s[6:7], s6, v12
	s_nop 0
	s_nop 0
	v_addc_co_u32_e64 v9, s[6:7], 0, v13, s[6:7]
	s_mov_b32 s6, 0x33000
	s_nop 0
	v_add_co_u32_e64 v16, s[6:7], s6, v12
	global_load_dwordx4 v[4:7], v[8:9], off offset:-4096 nt
	s_nop 0
	global_load_dwordx4 v[8:11], v[8:9], off nt
	v_addc_co_u32_e64 v17, s[6:7], 0, v13, s[6:7]
	global_load_dwordx4 v[12:15], v[16:17], off offset:-4096 nt
	s_nop 0
	global_load_dwordx4 v[16:19], v[16:17], off nt
	s_waitcnt vmcnt(15)
	v_mul_f32_e32 v2, 0x43800000, v52
	s_waitcnt vmcnt(14)
	v_mul_f32_e32 v52, 0x43800000, v56
	s_waitcnt vmcnt(13)
	v_mul_f32_e32 v56, 0x43800000, v60
	s_waitcnt vmcnt(12)
	v_mul_f32_e32 v60, 0x43800000, v64
	v_mov_b32_e32 v64, v3
	v_cvt_pk_fp8_f32 v64, v2, v52
	v_mul_f32_e32 v2, 0x43800000, v53
	v_mul_f32_e32 v52, 0x43800000, v57
	v_mov_b32_e32 v57, v3
	v_cvt_pk_fp8_f32 v57, v2, v52
	v_cvt_pk_fp8_f32 v64, v56, v60 op_sel:[0,0,1]
	v_mul_f32_e32 v53, 0x43800000, v61
	v_mul_f32_e32 v56, 0x43800000, v65
	v_cvt_pk_fp8_f32 v57, v53, v56 op_sel:[0,0,1]
	v_mul_f32_e32 v2, 0x43800000, v54
	v_mul_f32_e32 v52, 0x43800000, v58
	v_mov_b32_e32 v56, v3
	v_cvt_pk_fp8_f32 v56, v2, v52
	v_mul_f32_e32 v2, 0x43800000, v55
	v_mul_f32_e32 v52, 0x43800000, v59
	v_mov_b32_e32 v55, v3
	v_cvt_pk_fp8_f32 v55, v2, v52
	s_waitcnt vmcnt(11)
	v_mul_f32_e32 v2, 0x43800000, v36
	s_waitcnt vmcnt(10)
	v_mul_f32_e32 v36, 0x43800000, v40
	s_waitcnt vmcnt(9)
	v_mul_f32_e32 v40, 0x43800000, v44
	s_waitcnt vmcnt(8)
; #define LAS __attribute__((address_space(3)))
; __device__ __forceinline__ unsigned pk4_fp8(float a, float b, float c, float d) { unsigned w = 0u; w = __builtin_amdgcn_cvt_pk_fp8_f32(a, b, w, false); w = __builtin_amdgcn_cvt_pk_fp8_f32(c, d, w, true); return w; }
; __device__ __forceinline__ void conv_item8(const float* W, int K, int N, unsigned char* WT, int k0, int n0, int drow0, LAS unsigned* scr, int lane, float sc, bool rperm = false) {
;     ...
; #pragma unroll
;     for (int i = 0; i < 4; ++i) { const int rp = 4 * i + q; LAS unsigned* sp = scr + (4 * n4) * 17 + rp;
;         sp[0]  = pk4_fp8(v[i][0].x * sc, v[i][1].x * sc, v[i][2].x * sc, v[i][3].x * sc);
;         sp[17] = pk4_fp8(v[i][0].y * sc, v[i][1].y * sc, v[i][2].y * sc, v[i][3].y * sc);
;         sp[34] = pk4_fp8(v[i][0].z * sc, v[i][1].z * sc, v[i][2].z * sc, v[i][3].z * sc);
;         sp[51] = pk4_fp8(v[i][0].w * sc, v[i][1].w * sc, v[i][2].w * sc, v[i][3].w * sc); }
;     asm volatile("s_waitcnt lgkmcnt(0)" ::: "memory");
;     const int c = lane & 3;
; #pragma unroll
;     for (int j = 0; j < 4; ++j) {
;         const int n = (lane >> 2) + 16 * j; const LAS unsigned* sp = scr + n * 17 + 4 * c;
;         u32x4 o; o.x = sp[0]; o.y = sp[1]; o.z = sp[2]; o.w = sp[3];
;         const int nr = (rperm && n < 32) ? ((n < 16) ? 2 * n : 2 * (n - 16) + 1) : n;
;         *(u32x4*)(WT + (size_t)(drow0 + nr) * K + k0 + 16 * c) = o;
;     }
;     asm volatile("s_waitcnt lgkmcnt(0)" ::: "memory");
	v_mul_f32_e32 v44, 0x43800000, v48
	v_mov_b32_e32 v48, v3
	v_cvt_pk_fp8_f32 v48, v2, v36
	v_mul_f32_e32 v2, 0x43800000, v37
	v_mul_f32_e32 v36, 0x43800000, v41
	v_mov_b32_e32 v41, v3
	v_cvt_pk_fp8_f32 v41, v2, v36
	v_cvt_pk_fp8_f32 v48, v40, v44 op_sel:[0,0,1]
	v_mul_f32_e32 v37, 0x43800000, v45
	v_mul_f32_e32 v40, 0x43800000, v49
	v_cvt_pk_fp8_f32 v41, v37, v40 op_sel:[0,0,1]
	v_mul_f32_e32 v2, 0x43800000, v38
	v_mul_f32_e32 v36, 0x43800000, v42
	v_mov_b32_e32 v40, v3
	v_cvt_pk_fp8_f32 v40, v2, v36
	v_mul_f32_e32 v2, 0x43800000, v39
	v_mul_f32_e32 v36, 0x43800000, v43
	v_mov_b32_e32 v39, v3
	v_cvt_pk_fp8_f32 v39, v2, v36
	v_mul_f32_e32 v53, 0x43800000, v62
	v_mul_f32_e32 v54, 0x43800000, v66
	v_mul_f32_e32 v37, 0x43800000, v46
	v_mul_f32_e32 v38, 0x43800000, v50
	v_cvt_pk_fp8_f32 v56, v53, v54 op_sel:[0,0,1]
	v_mul_f32_e32 v53, 0x43800000, v63
	v_mul_f32_e32 v54, 0x43800000, v67
	v_cvt_pk_fp8_f32 v40, v37, v38 op_sel:[0,0,1]
	v_mul_f32_e32 v37, 0x43800000, v47
	v_mul_f32_e32 v38, 0x43800000, v51
	v_cvt_pk_fp8_f32 v55, v53, v54 op_sel:[0,0,1]
	v_cvt_pk_fp8_f32 v39, v37, v38 op_sel:[0,0,1]
	ds_write2_b32 v81, v64, v48 offset1:4
	ds_write2_b32 v81, v57, v41 offset0:17 offset1:21
	ds_write2_b32 v81, v56, v40 offset0:34 offset1:38
	ds_write2_b32 v81, v55, v39 offset0:51 offset1:55
	s_waitcnt vmcnt(7)
	v_mul_f32_e32 v2, 0x43800000, v20
	s_waitcnt vmcnt(6)
	v_mul_f32_e32 v20, 0x43800000, v24
	s_waitcnt vmcnt(5)
	v_mul_f32_e32 v24, 0x43800000, v28
	s_waitcnt vmcnt(4)
	v_mul_f32_e32 v28, 0x43800000, v32
	v_mov_b32_e32 v32, v3
	v_cvt_pk_fp8_f32 v32, v2, v20
	v_mul_f32_e32 v2, 0x43800000, v21
	v_mul_f32_e32 v20, 0x43800000, v25
	v_mov_b32_e32 v25, v3
	v_cvt_pk_fp8_f32 v25, v2, v20
	v_cvt_pk_fp8_f32 v32, v24, v28 op_sel:[0,0,1]
	v_mul_f32_e32 v21, 0x43800000, v29
	v_mul_f32_e32 v24, 0x43800000, v33
	v_cvt_pk_fp8_f32 v25, v21, v24 op_sel:[0,0,1]
	v_mul_f32_e32 v2, 0x43800000, v22
	v_mul_f32_e32 v20, 0x43800000, v26
	v_mov_b32_e32 v24, v3
	v_cvt_pk_fp8_f32 v24, v2, v20
	v_mul_f32_e32 v2, 0x43800000, v23
	v_mul_f32_e32 v20, 0x43800000, v27
	v_mov_b32_e32 v23, v3
	v_cvt_pk_fp8_f32 v23, v2, v20
	s_waitcnt vmcnt(3)
	v_mul_f32_e32 v2, 0x43800000, v4
	s_waitcnt vmcnt(2)
	v_mul_f32_e32 v4, 0x43800000, v8
	s_waitcnt vmcnt(1)
	v_mul_f32_e32 v8, 0x43800000, v12
	s_waitcnt vmcnt(0)
	v_mul_f32_e32 v12, 0x43800000, v16
	v_mov_b32_e32 v16, v3
	v_cvt_pk_fp8_f32 v16, v2, v4
	v_mul_f32_e32 v2, 0x43800000, v5
	v_mul_f32_e32 v4, 0x43800000, v9
	v_mov_b32_e32 v9, v3
	v_cvt_pk_fp8_f32 v9, v2, v4
	v_cvt_pk_fp8_f32 v16, v8, v12 op_sel:[0,0,1]
	v_mul_f32_e32 v5, 0x43800000, v13
	v_mul_f32_e32 v8, 0x43800000, v17
	v_cvt_pk_fp8_f32 v9, v5, v8 op_sel:[0,0,1]
	v_mul_f32_e32 v2, 0x43800000, v6
	v_mul_f32_e32 v4, 0x43800000, v10
	v_mov_b32_e32 v8, v3
	v_cvt_pk_fp8_f32 v8, v2, v4
	v_mul_f32_e32 v2, 0x43800000, v7
	v_mul_f32_e32 v4, 0x43800000, v11
	v_mov_b32_e32 v7, v3
	v_cvt_pk_fp8_f32 v7, v2, v4
	v_mul_f32_e32 v21, 0x43800000, v30
	v_mul_f32_e32 v22, 0x43800000, v34
	v_mul_f32_e32 v5, 0x43800000, v14
	v_mul_f32_e32 v6, 0x43800000, v18
	v_cvt_pk_fp8_f32 v24, v21, v22 op_sel:[0,0,1]
	v_mul_f32_e32 v21, 0x43800000, v31
	v_mul_f32_e32 v22, 0x43800000, v35
	v_cvt_pk_fp8_f32 v8, v5, v6 op_sel:[0,0,1]
	v_mul_f32_e32 v5, 0x43800000, v15
	v_mul_f32_e32 v6, 0x43800000, v19
	v_cvt_pk_fp8_f32 v23, v21, v22 op_sel:[0,0,1]
	v_cvt_pk_fp8_f32 v7, v5, v6 op_sel:[0,0,1]
	ds_write2_b32 v81, v32, v16 offset0:8 offset1:12
	ds_write2_b32 v81, v25, v9 offset0:25 offset1:29
	ds_write2_b32 v81, v24, v8 offset0:42 offset1:46
	ds_write2_b32 v81, v23, v7 offset0:59 offset1:63
	s_waitcnt lgkmcnt(0)
	v_lshl_add_u64 v[4:5], v[72:73], 0, v[74:75]
	v_lshl_add_u64 v[8:9], v[4:5], 0, v[68:69]
	ds_read2_b32 v[4:5], v88 offset1:1
	ds_read2_b32 v[6:7], v88 offset0:2 offset1:3
	v_or_b32_e32 v2, v76, v82
	v_lshlrev_b32_e32 v2, 11, v2
	v_lshl_add_u64 v[10:11], v[8:9], 0, v[2:3]
	v_or_b32_e32 v2, v76, v83
	s_waitcnt lgkmcnt(0)
	global_store_dwordx4 v[10:11], v[4:7], off
	ds_read2_b32 v[4:5], v89 offset1:1
	ds_read2_b32 v[6:7], v90 offset1:1
	v_lshlrev_b32_e32 v2, 11, v2
	v_lshl_add_u64 v[10:11], v[8:9], 0, v[2:3]
	v_or_b32_e32 v2, v76, v84
	v_lshlrev_b32_e32 v2, 11, v2
	s_waitcnt lgkmcnt(0)
	global_store_dwordx4 v[10:11], v[4:7], off
	ds_read2_b32 v[4:5], v91 offset1:1
	ds_read2_b32 v[6:7], v92 offset1:1
	v_lshl_add_u64 v[10:11], v[8:9], 0, v[2:3]
	v_or_b32_e32 v2, v76, v85
	v_lshlrev_b32_e32 v2, 11, v2
	v_lshl_add_u64 v[8:9], v[8:9], 0, v[2:3]
	s_waitcnt lgkmcnt(0)
	global_store_dwordx4 v[10:11], v[4:7], off
	ds_read2_b32 v[4:5], v93 offset1:1
	ds_read2_b32 v[6:7], v94 offset1:1
	s_waitcnt lgkmcnt(0)
	global_store_dwordx4 v[8:9], v[4:7], off
	s_waitcnt lgkmcnt(0)
